# v102 + pool/conv pass: PROJ window loads marked nt (streaming; keep q/k/v/indexer columns of PROJ in L2 for the scores and attention phases)
# speedup vs baseline: 1.0041x; 1.0019x over previous
; __device__ __forceinline__ unsigned pk2(float lo, float hi) { return pg8::cvt_pk_bf16(lo, hi); }
; __device__ __forceinline__ void unpack8(const v4u w, float (&f)[8]) { f[0] = bflo(w.x); f[1] = bfhi(w.x); f[2] = bflo(w.y); f[3] = bfhi(w.y); f[4] = bflo(w.z); f[5] = bfhi(w.z); f[6] = bflo(w.w); f[7] = bfhi(w.w); }
; __device__ __forceinline__ int lane_id() { int l; asm volatile("s_nop 4\n\tv_mbcnt_lo_u32_b32 %0, -1, 0\n\tv_mbcnt_hi_u32_b32 %0, -1, %0\n\ts_nop 4" : "=v"(l)); return l; }
; template <int W> __device__ __forceinline__ void pool_item(Frame& F, int row, int t, int c8) {
;     float s[8], u[8];
; #pragma unroll
;     for (int i = 0; i < 8; ++i) s[i] = 0.f;
;     v4u ld[W];
; #pragma unroll
;     for (int k = 0; k < W; ++k) { const int kk = (t - k) >= 0 ? k : t; ld[k] = *(const v4u*)(F.PROJ + (size_t)(row - kk) * INWP + O_UPOOL + c8); }
; #pragma unroll
;     for (int k = W - 1; k >= 0; --k) { unpack8(ld[k], u); const float wgt = (t - k) >= 0 ? 1.f : 0.f;
; #pragma unroll
;         for (int i = 0; i < 8; ++i) s[i] += wgt * u[i]; }
;     const int cnt = (t + 1) < W ? (t + 1) : W;
;     const float inv = 1.0f / (float)cnt;
;     v4u o; o.x = pk2(s[0] * inv - u[0], s[1] * inv - u[1]); o.y = pk2(s[2] * inv - u[2], s[3] * inv - u[3]); o.z = pk2(s[4] * inv - u[4], s[5] * inv - u[5]); o.w = pk2(s[6] * inv - u[6], s[7] * inv - u[7]);
;     *(v4u*)(F.Y + (size_t)row * 1024 + c8) = o;
; }
; __device__ __forceinline__ void poolconv_phase(Frame& F, const float* conv_w_l) {
;     int tid = F.wave * 64 + lane_id(); asm volatile("" : "+v"(tid));
;     const int gt = F.vcu * NTHR + tid, NGT = F.G * NTHR;
;     for (int idx = gt; idx < M * 128; idx += NGT) {
;         const int grp = idx / (M * 32), rem = idx - grp * (M * 32), row = rem >> 5, c8 = grp * 256 + (rem & 31) * 8, t = row & (SEQ - 1);
;         if (grp == 0) pool_item<2>(F, row, t, c8); else if (grp == 1) pool_item<4>(F, row, t, c8); else if (grp == 2) pool_item<8>(F, row, t, c8); else pool_item<16>(F, row, t, c8);
;     }
.LBB0_239:
	v_readlane_b32 s0, v255, 42
	s_add_i32 s4, s0, 2
	v_readlane_b32 s0, v251, 14
	v_readlane_b32 s1, v251, 15
	s_cmp_le_i32 s0, s4
	s_cselect_b64 s[2:3], -1, 0
	s_cmp_lt_i32 s4, s1
	s_cselect_b64 s[4:5], -1, 0
	s_mov_b32 s1, s63
	s_and_b64 s[2:3], s[2:3], s[4:5]
	v_writelane_b32 v255, s0, 45
	s_andn2_b64 vcc, exec, s[2:3]
	s_nop 0
	v_writelane_b32 v255, s1, 46
	s_cbranch_vccnz .LBB0_540
	v_mbcnt_lo_u32_b32 v0, -1, 0
	v_mbcnt_hi_u32_b32 v0, -1, v0
	v_readlane_b32 s0, v255, 12
	v_readlane_b32 s14, v251, 40
	v_readlane_b32 s15, v251, 41
	v_readlane_b32 s10, v255, 43
	s_and_b32 s1, s0, 7
	s_lshl_b32 s1, s1, 5
	s_lshr_b32 s0, s0, 3
	s_or_b32 s1, s1, s0
	s_lshl_b32 s2, s1, 9
	s_lshl_b32 s3, s35, 6
	s_add_i32 s2, s2, s3
	v_add_u32_e32 v1, s2, v0
	s_lshr_b32 s3, s1, 7
	v_and_b32_e32 v2, 0xffff, v1
	v_lshrrev_b32_e32 v2, 5, v2
	v_and_b32_e32 v3, 31, v1
	v_lshlrev_b32_e32 v4, 2, v2
	v_and_b32_e32 v5, 0x7ff, v4
	v_mul_u32_u24_e32 v6, 0x3600, v5
	v_mul_u32_u24_e32 v7, 0x3600, v4
	v_lshlrev_b32_e32 v8, 4, v3
	v_lshl_add_u32 v9, v4, 11, v8
	v_add_u32_e32 v7, v7, v8
	s_cmp_eq_u32 s3, 0
	s_cbranch_scc0 .Lpc_g1
	v_add_u32_e32 v14, 0x0, v7
	v_add_u32_e32 v15, 0x600, v7
	v_add_u32_e32 v16, 0x0, v9
	v_add_u32_e32 v17, 0x600, v9
	v_min_u32_e32 v11, 0x3600, v6
	v_sub_u32_e32 v12, v14, v11
	global_load_dwordx4 v[20:23], v12, s[96:97] nt
	global_load_dwordx4 v[24:27], v14, s[96:97] nt
	v_add_u32_e32 v12, 0x3600, v14
	global_load_dwordx4 v[28:31], v12, s[96:97] nt
	v_add_u32_e32 v12, 0x6c00, v14
	global_load_dwordx4 v[32:35], v12, s[96:97] nt
	v_add_u32_e32 v12, 0xa200, v14
	global_load_dwordx4 v[36:39], v12, s[96:97] nt
	v_min_u32_e32 v11, 0x32a00, v6
	v_sub_u32_e32 v12, v15, v11
	global_load_dwordx4 v[48:51], v12, s[96:97] nt
	v_min_u32_e32 v11, 0x2f400, v6
	v_sub_u32_e32 v12, v15, v11
	global_load_dwordx4 v[52:55], v12, s[96:97] nt
	v_min_u32_e32 v11, 0x2be00, v6
	v_sub_u32_e32 v12, v15, v11
	global_load_dwordx4 v[56:59], v12, s[96:97] nt
	v_min_u32_e32 v11, 0x28800, v6
	v_sub_u32_e32 v12, v15, v11
	global_load_dwordx4 v[60:63], v12, s[96:97] nt
	v_min_u32_e32 v11, 0x25200, v6
	v_sub_u32_e32 v12, v15, v11
	global_load_dwordx4 v[64:67], v12, s[96:97] nt
	v_min_u32_e32 v11, 0x21c00, v6
	v_sub_u32_e32 v12, v15, v11
	global_load_dwordx4 v[68:71], v12, s[96:97] nt
	v_min_u32_e32 v11, 0x1e600, v6
	v_sub_u32_e32 v12, v15, v11
	global_load_dwordx4 v[72:75], v12, s[96:97] nt
	v_min_u32_e32 v11, 0x1b000, v6
	v_sub_u32_e32 v12, v15, v11
	global_load_dwordx4 v[76:79], v12, s[96:97] nt
	v_min_u32_e32 v11, 0x17a00, v6
	v_sub_u32_e32 v12, v15, v11
	global_load_dwordx4 v[80:83], v12, s[96:97] nt
	v_min_u32_e32 v11, 0x14400, v6
	v_sub_u32_e32 v12, v15, v11
	global_load_dwordx4 v[84:87], v12, s[96:97] nt
	v_min_u32_e32 v11, 0x10e00, v6
	v_sub_u32_e32 v12, v15, v11
	global_load_dwordx4 v[88:91], v12, s[96:97] nt
	v_min_u32_e32 v11, 0xd800, v6
	v_sub_u32_e32 v12, v15, v11
	global_load_dwordx4 v[92:95], v12, s[96:97] nt
	v_min_u32_e32 v11, 0xa200, v6
	v_sub_u32_e32 v12, v15, v11
	global_load_dwordx4 v[96:99], v12, s[96:97] nt
	v_min_u32_e32 v11, 0x6c00, v6
	v_sub_u32_e32 v12, v15, v11
	global_load_dwordx4 v[100:103], v12, s[96:97] nt
	v_min_u32_e32 v11, 0x3600, v6
	v_sub_u32_e32 v12, v15, v11
	global_load_dwordx4 v[104:107], v12, s[96:97] nt
	global_load_dwordx4 v[108:111], v15, s[96:97] nt
	v_add_u32_e32 v12, 0x3600, v15
	global_load_dwordx4 v[112:115], v12, s[96:97] nt
	v_add_u32_e32 v12, 0x6c00, v15
	global_load_dwordx4 v[116:119], v12, s[96:97] nt
	v_add_u32_e32 v12, 0xa200, v15
	global_load_dwordx4 v[120:123], v12, s[96:97] nt
	s_waitcnt vmcnt(19)
	v_cmp_le_u32_e32 vcc, 1, v5
	s_nop 1
	v_cndmask_b32_e32 v20, 0, v20, vcc
	v_cndmask_b32_e32 v21, 0, v21, vcc
	v_cndmask_b32_e32 v22, 0, v22, vcc
	v_cndmask_b32_e32 v23, 0, v23, vcc
	v_add_u32_e32 v226, 1, v5
	v_min_u32_e32 v226, 2, v226
	v_cvt_f32_u32_e32 v226, v226
	v_rcp_f32_e32 v226, v226
	v_add_u32_e32 v227, 2, v5
	v_min_u32_e32 v227, 2, v227
	v_cvt_f32_u32_e32 v227, v227
	v_rcp_f32_e32 v227, v227
	v_add_u32_e32 v228, 3, v5
	v_min_u32_e32 v228, 2, v228
	v_cvt_f32_u32_e32 v228, v228
	v_rcp_f32_e32 v228, v228
	v_add_u32_e32 v229, 4, v5
	v_min_u32_e32 v229, 2, v229
	v_cvt_f32_u32_e32 v229, v229
	v_rcp_f32_e32 v229, v229
	v_lshlrev_b32_e32 v124, 16, v20
	v_and_b32_e32 v125, 0xffff0000, v20
	v_lshlrev_b32_e32 v126, 16, v24
	v_and_b32_e32 v127, 0xffff0000, v24
	v_lshlrev_b32_e32 v128, 16, v28
	v_and_b32_e32 v129, 0xffff0000, v28
	v_lshlrev_b32_e32 v130, 16, v32
	v_and_b32_e32 v131, 0xffff0000, v32
	v_lshlrev_b32_e32 v132, 16, v36
	v_and_b32_e32 v133, 0xffff0000, v36
	v_add_f32_e32 v194, v124, v126
	v_fma_f32 v194, v194, v226, -v126
	v_add_f32_e32 v195, v125, v127
	v_fma_f32 v195, v195, v226, -v127
	v_add_f32_e32 v202, v126, v128
	v_fma_f32 v202, v202, v227, -v128
	v_add_f32_e32 v203, v127, v129
	v_fma_f32 v203, v203, v227, -v129
	v_add_f32_e32 v210, v128, v130
	v_fma_f32 v210, v210, v228, -v130
	v_add_f32_e32 v211, v129, v131
	v_fma_f32 v211, v211, v228, -v131
	v_add_f32_e32 v218, v130, v132
	v_fma_f32 v218, v218, v229, -v132
	v_add_f32_e32 v219, v131, v133
	v_fma_f32 v219, v219, v229, -v133
	v_lshlrev_b32_e32 v124, 16, v21
	v_and_b32_e32 v125, 0xffff0000, v21
	v_lshlrev_b32_e32 v126, 16, v25
	v_and_b32_e32 v127, 0xffff0000, v25
	v_lshlrev_b32_e32 v128, 16, v29
	v_and_b32_e32 v129, 0xffff0000, v29
	v_lshlrev_b32_e32 v130, 16, v33
	v_and_b32_e32 v131, 0xffff0000, v33
	v_lshlrev_b32_e32 v132, 16, v37
	v_and_b32_e32 v133, 0xffff0000, v37
	v_add_f32_e32 v196, v124, v126
	v_fma_f32 v196, v196, v226, -v126
	v_add_f32_e32 v197, v125, v127
	v_fma_f32 v197, v197, v226, -v127
	v_add_f32_e32 v204, v126, v128
	v_fma_f32 v204, v204, v227, -v128
; __device__ __forceinline__ unsigned pk2(float lo, float hi) { return pg8::cvt_pk_bf16(lo, hi); }
; __device__ __forceinline__ void unpack8(const v4u w, float (&f)[8]) { f[0] = bflo(w.x); f[1] = bfhi(w.x); f[2] = bflo(w.y); f[3] = bfhi(w.y); f[4] = bflo(w.z); f[5] = bfhi(w.z); f[6] = bflo(w.w); f[7] = bfhi(w.w); }
; template <int W> __device__ __forceinline__ void pool_item(Frame& F, int row, int t, int c8) {
;     ...
;     for (int k = 0; k < W; ++k) { const int kk = (t - k) >= 0 ? k : t; ld[k] = *(const v4u*)(F.PROJ + (size_t)(row - kk) * INWP + O_UPOOL + c8); }
; #pragma unroll
;     for (int k = W - 1; k >= 0; --k) { unpack8(ld[k], u); const float wgt = (t - k) >= 0 ? 1.f : 0.f;
; #pragma unroll
;         for (int i = 0; i < 8; ++i) s[i] += wgt * u[i]; }
;     const int cnt = (t + 1) < W ? (t + 1) : W;
;     const float inv = 1.0f / (float)cnt;
;     v4u o; o.x = pk2(s[0] * inv - u[0], s[1] * inv - u[1]); o.y = pk2(s[2] * inv - u[2], s[3] * inv - u[3]); o.z = pk2(s[4] * inv - u[4], s[5] * inv - u[5]); o.w = pk2(s[6] * inv - u[6], s[7] * inv - u[7]);
;     *(v4u*)(F.Y + (size_t)row * 1024 + c8) = o;
	v_add_f32_e32 v205, v127, v129
	v_fma_f32 v205, v205, v227, -v129
	v_add_f32_e32 v212, v128, v130
	v_fma_f32 v212, v212, v228, -v130
	v_add_f32_e32 v213, v129, v131
	v_fma_f32 v213, v213, v228, -v131
	v_add_f32_e32 v220, v130, v132
	v_fma_f32 v220, v220, v229, -v132
	v_add_f32_e32 v221, v131, v133
	v_fma_f32 v221, v221, v229, -v133
	v_lshlrev_b32_e32 v124, 16, v22
	v_and_b32_e32 v125, 0xffff0000, v22
	v_lshlrev_b32_e32 v126, 16, v26
	v_and_b32_e32 v127, 0xffff0000, v26
	v_lshlrev_b32_e32 v128, 16, v30
	v_and_b32_e32 v129, 0xffff0000, v30
	v_lshlrev_b32_e32 v130, 16, v34
	v_and_b32_e32 v131, 0xffff0000, v34
	v_lshlrev_b32_e32 v132, 16, v38
	v_and_b32_e32 v133, 0xffff0000, v38
	v_add_f32_e32 v198, v124, v126
	v_fma_f32 v198, v198, v226, -v126
	v_add_f32_e32 v199, v125, v127
	v_fma_f32 v199, v199, v226, -v127
	v_add_f32_e32 v206, v126, v128
	v_fma_f32 v206, v206, v227, -v128
	v_add_f32_e32 v207, v127, v129
	v_fma_f32 v207, v207, v227, -v129
	v_add_f32_e32 v214, v128, v130
	v_fma_f32 v214, v214, v228, -v130
	v_add_f32_e32 v215, v129, v131
	v_fma_f32 v215, v215, v228, -v131
	v_add_f32_e32 v222, v130, v132
	v_fma_f32 v222, v222, v229, -v132
	v_add_f32_e32 v223, v131, v133
	v_fma_f32 v223, v223, v229, -v133
	v_lshlrev_b32_e32 v124, 16, v23
	v_and_b32_e32 v125, 0xffff0000, v23
	v_lshlrev_b32_e32 v126, 16, v27
	v_and_b32_e32 v127, 0xffff0000, v27
	v_lshlrev_b32_e32 v128, 16, v31
	v_and_b32_e32 v129, 0xffff0000, v31
	v_lshlrev_b32_e32 v130, 16, v35
	v_and_b32_e32 v131, 0xffff0000, v35
	v_lshlrev_b32_e32 v132, 16, v39
	v_and_b32_e32 v133, 0xffff0000, v39
	v_add_f32_e32 v200, v124, v126
	v_fma_f32 v200, v200, v226, -v126
	v_add_f32_e32 v201, v125, v127
	v_fma_f32 v201, v201, v226, -v127
	v_add_f32_e32 v208, v126, v128
	v_fma_f32 v208, v208, v227, -v128
	v_add_f32_e32 v209, v127, v129
	v_fma_f32 v209, v209, v227, -v129
	v_add_f32_e32 v216, v128, v130
	v_fma_f32 v216, v216, v228, -v130
	v_add_f32_e32 v217, v129, v131
	v_fma_f32 v217, v217, v228, -v131
	v_add_f32_e32 v224, v130, v132
	v_fma_f32 v224, v224, v229, -v132
	v_add_f32_e32 v225, v131, v133
	v_fma_f32 v225, v225, v229, -v133
	v_cvt_pk_bf16_f32 v194, v194, v195
	v_cvt_pk_bf16_f32 v195, v196, v197
	v_cvt_pk_bf16_f32 v196, v198, v199
	v_cvt_pk_bf16_f32 v197, v200, v201
	global_store_dwordx4 v16, v[194:197], s[14:15]
	v_cvt_pk_bf16_f32 v202, v202, v203
	v_cvt_pk_bf16_f32 v203, v204, v205
	v_cvt_pk_bf16_f32 v204, v206, v207
	v_cvt_pk_bf16_f32 v205, v208, v209
	v_add_u32_e32 v13, 0x800, v16
	global_store_dwordx4 v13, v[202:205], s[14:15]
	v_cvt_pk_bf16_f32 v210, v210, v211
	v_cvt_pk_bf16_f32 v211, v212, v213
	v_cvt_pk_bf16_f32 v212, v214, v215
	v_cvt_pk_bf16_f32 v213, v216, v217
	v_add_u32_e32 v13, 0x1000, v16
	global_store_dwordx4 v13, v[210:213], s[14:15]
	v_cvt_pk_bf16_f32 v218, v218, v219
	v_cvt_pk_bf16_f32 v219, v220, v221
	v_cvt_pk_bf16_f32 v220, v222, v223
	v_cvt_pk_bf16_f32 v221, v224, v225
	v_add_u32_e32 v13, 0x1800, v16
	global_store_dwordx4 v13, v[218:221], s[14:15]
	s_waitcnt vmcnt(4)
	v_cmp_le_u32_e32 vcc, 15, v5
	s_nop 1
	v_cndmask_b32_e32 v48, 0, v48, vcc
	v_cndmask_b32_e32 v49, 0, v49, vcc
	v_cndmask_b32_e32 v50, 0, v50, vcc
	v_cndmask_b32_e32 v51, 0, v51, vcc
	v_cmp_le_u32_e32 vcc, 14, v5
	s_nop 1
	v_cndmask_b32_e32 v52, 0, v52, vcc
	v_cndmask_b32_e32 v53, 0, v53, vcc
	v_cndmask_b32_e32 v54, 0, v54, vcc
	v_cndmask_b32_e32 v55, 0, v55, vcc
	v_cmp_le_u32_e32 vcc, 13, v5
	s_nop 1
	v_cndmask_b32_e32 v56, 0, v56, vcc
	v_cndmask_b32_e32 v57, 0, v57, vcc
	v_cndmask_b32_e32 v58, 0, v58, vcc
	v_cndmask_b32_e32 v59, 0, v59, vcc
	v_cmp_le_u32_e32 vcc, 12, v5
	s_nop 1
	v_cndmask_b32_e32 v60, 0, v60, vcc
	v_cndmask_b32_e32 v61, 0, v61, vcc
	v_cndmask_b32_e32 v62, 0, v62, vcc
	v_cndmask_b32_e32 v63, 0, v63, vcc
	v_cmp_le_u32_e32 vcc, 11, v5
	s_nop 1
	v_cndmask_b32_e32 v64, 0, v64, vcc
	v_cndmask_b32_e32 v65, 0, v65, vcc
	v_cndmask_b32_e32 v66, 0, v66, vcc
	v_cndmask_b32_e32 v67, 0, v67, vcc
	v_cmp_le_u32_e32 vcc, 10, v5
	s_nop 1
	v_cndmask_b32_e32 v68, 0, v68, vcc
	v_cndmask_b32_e32 v69, 0, v69, vcc
	v_cndmask_b32_e32 v70, 0, v70, vcc
	v_cndmask_b32_e32 v71, 0, v71, vcc
	v_cmp_le_u32_e32 vcc, 9, v5
	s_nop 1
	v_cndmask_b32_e32 v72, 0, v72, vcc
	v_cndmask_b32_e32 v73, 0, v73, vcc
	v_cndmask_b32_e32 v74, 0, v74, vcc
	v_cndmask_b32_e32 v75, 0, v75, vcc
	v_cmp_le_u32_e32 vcc, 8, v5
	s_nop 1
	v_cndmask_b32_e32 v76, 0, v76, vcc
	v_cndmask_b32_e32 v77, 0, v77, vcc
	v_cndmask_b32_e32 v78, 0, v78, vcc
	v_cndmask_b32_e32 v79, 0, v79, vcc
	v_cmp_le_u32_e32 vcc, 7, v5
	s_nop 1
	v_cndmask_b32_e32 v80, 0, v80, vcc
	v_cndmask_b32_e32 v81, 0, v81, vcc
	v_cndmask_b32_e32 v82, 0, v82, vcc
	v_cndmask_b32_e32 v83, 0, v83, vcc
	v_cmp_le_u32_e32 vcc, 6, v5
	s_nop 1
	v_cndmask_b32_e32 v84, 0, v84, vcc
	v_cndmask_b32_e32 v85, 0, v85, vcc
	v_cndmask_b32_e32 v86, 0, v86, vcc
	v_cndmask_b32_e32 v87, 0, v87, vcc
	v_cmp_le_u32_e32 vcc, 5, v5
	s_nop 1
	v_cndmask_b32_e32 v88, 0, v88, vcc
	v_cndmask_b32_e32 v89, 0, v89, vcc
	v_cndmask_b32_e32 v90, 0, v90, vcc
	v_cndmask_b32_e32 v91, 0, v91, vcc
	v_cmp_le_u32_e32 vcc, 4, v5
	s_nop 1
	v_cndmask_b32_e32 v92, 0, v92, vcc
	v_cndmask_b32_e32 v93, 0, v93, vcc
	v_cndmask_b32_e32 v94, 0, v94, vcc
	v_cndmask_b32_e32 v95, 0, v95, vcc
	v_cmp_le_u32_e32 vcc, 3, v5
	s_nop 1
	v_cndmask_b32_e32 v96, 0, v96, vcc
	v_cndmask_b32_e32 v97, 0, v97, vcc
	v_cndmask_b32_e32 v98, 0, v98, vcc
	v_cndmask_b32_e32 v99, 0, v99, vcc
	v_cmp_le_u32_e32 vcc, 2, v5
	s_nop 1
	v_cndmask_b32_e32 v100, 0, v100, vcc
	v_cndmask_b32_e32 v101, 0, v101, vcc
	v_cndmask_b32_e32 v102, 0, v102, vcc
	v_cndmask_b32_e32 v103, 0, v103, vcc
	v_cmp_le_u32_e32 vcc, 1, v5
	s_nop 1
	v_cndmask_b32_e32 v104, 0, v104, vcc
; __device__ __forceinline__ unsigned pk2(float lo, float hi) { return pg8::cvt_pk_bf16(lo, hi); }
; __device__ __forceinline__ void unpack8(const v4u w, float (&f)[8]) { f[0] = bflo(w.x); f[1] = bfhi(w.x); f[2] = bflo(w.y); f[3] = bfhi(w.y); f[4] = bflo(w.z); f[5] = bfhi(w.z); f[6] = bflo(w.w); f[7] = bfhi(w.w); }
; template <int W> __device__ __forceinline__ void pool_item(Frame& F, int row, int t, int c8) {
;     ...
;     for (int k = 0; k < W; ++k) { const int kk = (t - k) >= 0 ? k : t; ld[k] = *(const v4u*)(F.PROJ + (size_t)(row - kk) * INWP + O_UPOOL + c8); }
; #pragma unroll
;     for (int k = W - 1; k >= 0; --k) { unpack8(ld[k], u); const float wgt = (t - k) >= 0 ? 1.f : 0.f;
; #pragma unroll
;         for (int i = 0; i < 8; ++i) s[i] += wgt * u[i]; }
;     const int cnt = (t + 1) < W ? (t + 1) : W;
;     const float inv = 1.0f / (float)cnt;
;     v4u o; o.x = pk2(s[0] * inv - u[0], s[1] * inv - u[1]); o.y = pk2(s[2] * inv - u[2], s[3] * inv - u[3]); o.z = pk2(s[4] * inv - u[4], s[5] * inv - u[5]); o.w = pk2(s[6] * inv - u[6], s[7] * inv - u[7]);
	v_cndmask_b32_e32 v105, 0, v105, vcc
	v_cndmask_b32_e32 v106, 0, v106, vcc
	v_cndmask_b32_e32 v107, 0, v107, vcc
	v_add_u32_e32 v226, 1, v5
	v_min_u32_e32 v226, 16, v226
	v_cvt_f32_u32_e32 v226, v226
	v_rcp_f32_e32 v226, v226
	v_add_u32_e32 v227, 2, v5
	v_min_u32_e32 v227, 16, v227
	v_cvt_f32_u32_e32 v227, v227
	v_rcp_f32_e32 v227, v227
	v_add_u32_e32 v228, 3, v5
	v_min_u32_e32 v228, 16, v228
	v_cvt_f32_u32_e32 v228, v228
	v_rcp_f32_e32 v228, v228
	v_add_u32_e32 v229, 4, v5
	v_min_u32_e32 v229, 16, v229
	v_cvt_f32_u32_e32 v229, v229
	v_rcp_f32_e32 v229, v229
	v_lshlrev_b32_e32 v124, 16, v48
	v_and_b32_e32 v125, 0xffff0000, v48
	v_lshlrev_b32_e32 v126, 16, v52
	v_and_b32_e32 v127, 0xffff0000, v52
	v_lshlrev_b32_e32 v128, 16, v56
	v_and_b32_e32 v129, 0xffff0000, v56
	v_lshlrev_b32_e32 v130, 16, v60
	v_and_b32_e32 v131, 0xffff0000, v60
	v_lshlrev_b32_e32 v132, 16, v64
	v_and_b32_e32 v133, 0xffff0000, v64
	v_lshlrev_b32_e32 v134, 16, v68
	v_and_b32_e32 v135, 0xffff0000, v68
	v_lshlrev_b32_e32 v136, 16, v72
	v_and_b32_e32 v137, 0xffff0000, v72
	v_lshlrev_b32_e32 v138, 16, v76
	v_and_b32_e32 v139, 0xffff0000, v76
	v_lshlrev_b32_e32 v140, 16, v80
	v_and_b32_e32 v141, 0xffff0000, v80
	v_lshlrev_b32_e32 v142, 16, v84
	v_and_b32_e32 v143, 0xffff0000, v84
	v_lshlrev_b32_e32 v144, 16, v88
	v_and_b32_e32 v145, 0xffff0000, v88
	v_lshlrev_b32_e32 v146, 16, v92
	v_and_b32_e32 v147, 0xffff0000, v92
	v_lshlrev_b32_e32 v148, 16, v96
	v_and_b32_e32 v149, 0xffff0000, v96
	v_lshlrev_b32_e32 v150, 16, v100
	v_and_b32_e32 v151, 0xffff0000, v100
	v_lshlrev_b32_e32 v152, 16, v104
	v_and_b32_e32 v153, 0xffff0000, v104
	v_lshlrev_b32_e32 v154, 16, v108
	v_and_b32_e32 v155, 0xffff0000, v108
	v_lshlrev_b32_e32 v156, 16, v112
	v_and_b32_e32 v157, 0xffff0000, v112
	v_lshlrev_b32_e32 v158, 16, v116
	v_and_b32_e32 v159, 0xffff0000, v116
	v_lshlrev_b32_e32 v160, 16, v120
	v_and_b32_e32 v161, 0xffff0000, v120
	v_add_f32_e32 v194, v124, v126
	v_add_f32_e32 v194, v194, v128
	v_add_f32_e32 v194, v194, v130
	v_add_f32_e32 v194, v194, v132
	v_add_f32_e32 v194, v194, v134
	v_add_f32_e32 v194, v194, v136
	v_add_f32_e32 v194, v194, v138
	v_add_f32_e32 v194, v194, v140
	v_add_f32_e32 v194, v194, v142
	v_add_f32_e32 v194, v194, v144
	v_add_f32_e32 v194, v194, v146
	v_add_f32_e32 v194, v194, v148
	v_add_f32_e32 v194, v194, v150
	v_add_f32_e32 v194, v194, v152
	v_add_f32_e32 v194, v194, v154
	v_fma_f32 v194, v194, v226, -v154
	v_add_f32_e32 v195, v125, v127
	v_add_f32_e32 v195, v195, v129
	v_add_f32_e32 v195, v195, v131
	v_add_f32_e32 v195, v195, v133
	v_add_f32_e32 v195, v195, v135
	v_add_f32_e32 v195, v195, v137
	v_add_f32_e32 v195, v195, v139
	v_add_f32_e32 v195, v195, v141
	v_add_f32_e32 v195, v195, v143
	v_add_f32_e32 v195, v195, v145
	v_add_f32_e32 v195, v195, v147
	v_add_f32_e32 v195, v195, v149
	v_add_f32_e32 v195, v195, v151
	v_add_f32_e32 v195, v195, v153
	v_add_f32_e32 v195, v195, v155
	v_fma_f32 v195, v195, v226, -v155
	v_add_f32_e32 v202, v126, v128
	v_add_f32_e32 v202, v202, v130
	v_add_f32_e32 v202, v202, v132
	v_add_f32_e32 v202, v202, v134
	v_add_f32_e32 v202, v202, v136
	v_add_f32_e32 v202, v202, v138
	v_add_f32_e32 v202, v202, v140
	v_add_f32_e32 v202, v202, v142
	v_add_f32_e32 v202, v202, v144
	v_add_f32_e32 v202, v202, v146
	v_add_f32_e32 v202, v202, v148
	v_add_f32_e32 v202, v202, v150
	v_add_f32_e32 v202, v202, v152
	v_add_f32_e32 v202, v202, v154
	v_add_f32_e32 v202, v202, v156
	v_fma_f32 v202, v202, v227, -v156
	v_add_f32_e32 v203, v127, v129
	v_add_f32_e32 v203, v203, v131
	v_add_f32_e32 v203, v203, v133
	v_add_f32_e32 v203, v203, v135
	v_add_f32_e32 v203, v203, v137
	v_add_f32_e32 v203, v203, v139
	v_add_f32_e32 v203, v203, v141
	v_add_f32_e32 v203, v203, v143
	v_add_f32_e32 v203, v203, v145
	v_add_f32_e32 v203, v203, v147
	v_add_f32_e32 v203, v203, v149
	v_add_f32_e32 v203, v203, v151
	v_add_f32_e32 v203, v203, v153
	v_add_f32_e32 v203, v203, v155
	v_add_f32_e32 v203, v203, v157
	v_fma_f32 v203, v203, v227, -v157
	v_add_f32_e32 v210, v128, v130
	v_add_f32_e32 v210, v210, v132
	v_add_f32_e32 v210, v210, v134
	v_add_f32_e32 v210, v210, v136
	v_add_f32_e32 v210, v210, v138
	v_add_f32_e32 v210, v210, v140
	v_add_f32_e32 v210, v210, v142
	v_add_f32_e32 v210, v210, v144
	v_add_f32_e32 v210, v210, v146
	v_add_f32_e32 v210, v210, v148
	v_add_f32_e32 v210, v210, v150
	v_add_f32_e32 v210, v210, v152
	v_add_f32_e32 v210, v210, v154
	v_add_f32_e32 v210, v210, v156
	v_add_f32_e32 v210, v210, v158
	v_fma_f32 v210, v210, v228, -v158
	v_add_f32_e32 v211, v129, v131
	v_add_f32_e32 v211, v211, v133
	v_add_f32_e32 v211, v211, v135
	v_add_f32_e32 v211, v211, v137
	v_add_f32_e32 v211, v211, v139
	v_add_f32_e32 v211, v211, v141
	v_add_f32_e32 v211, v211, v143
	v_add_f32_e32 v211, v211, v145
	v_add_f32_e32 v211, v211, v147
	v_add_f32_e32 v211, v211, v149
	v_add_f32_e32 v211, v211, v151
	v_add_f32_e32 v211, v211, v153
	v_add_f32_e32 v211, v211, v155
	v_add_f32_e32 v211, v211, v157
	v_add_f32_e32 v211, v211, v159
	v_fma_f32 v211, v211, v228, -v159
	v_add_f32_e32 v218, v130, v132
	v_add_f32_e32 v218, v218, v134
	v_add_f32_e32 v218, v218, v136
	v_add_f32_e32 v218, v218, v138
	v_add_f32_e32 v218, v218, v140
	v_add_f32_e32 v218, v218, v142
	v_add_f32_e32 v218, v218, v144
	v_add_f32_e32 v218, v218, v146
	v_add_f32_e32 v218, v218, v148
	v_add_f32_e32 v218, v218, v150
	v_add_f32_e32 v218, v218, v152
	v_add_f32_e32 v218, v218, v154
	v_add_f32_e32 v218, v218, v156
	v_add_f32_e32 v218, v218, v158
	v_add_f32_e32 v218, v218, v160
	v_fma_f32 v218, v218, v229, -v160
	v_add_f32_e32 v219, v131, v133
	v_add_f32_e32 v219, v219, v135
	v_add_f32_e32 v219, v219, v137
	v_add_f32_e32 v219, v219, v139
; __device__ __forceinline__ unsigned pk2(float lo, float hi) { return pg8::cvt_pk_bf16(lo, hi); }
; __device__ __forceinline__ void unpack8(const v4u w, float (&f)[8]) { f[0] = bflo(w.x); f[1] = bfhi(w.x); f[2] = bflo(w.y); f[3] = bfhi(w.y); f[4] = bflo(w.z); f[5] = bfhi(w.z); f[6] = bflo(w.w); f[7] = bfhi(w.w); }
; template <int W> __device__ __forceinline__ void pool_item(Frame& F, int row, int t, int c8) {
;     ...
;     for (int k = 0; k < W; ++k) { const int kk = (t - k) >= 0 ? k : t; ld[k] = *(const v4u*)(F.PROJ + (size_t)(row - kk) * INWP + O_UPOOL + c8); }
; #pragma unroll
;     for (int k = W - 1; k >= 0; --k) { unpack8(ld[k], u); const float wgt = (t - k) >= 0 ? 1.f : 0.f;
; #pragma unroll
;         for (int i = 0; i < 8; ++i) s[i] += wgt * u[i]; }
;     const int cnt = (t + 1) < W ? (t + 1) : W;
;     const float inv = 1.0f / (float)cnt;
;     v4u o; o.x = pk2(s[0] * inv - u[0], s[1] * inv - u[1]); o.y = pk2(s[2] * inv - u[2], s[3] * inv - u[3]); o.z = pk2(s[4] * inv - u[4], s[5] * inv - u[5]); o.w = pk2(s[6] * inv - u[6], s[7] * inv - u[7]);
	v_add_f32_e32 v219, v219, v141
	v_add_f32_e32 v219, v219, v143
	v_add_f32_e32 v219, v219, v145
	v_add_f32_e32 v219, v219, v147
	v_add_f32_e32 v219, v219, v149
	v_add_f32_e32 v219, v219, v151
	v_add_f32_e32 v219, v219, v153
	v_add_f32_e32 v219, v219, v155
	v_add_f32_e32 v219, v219, v157
	v_add_f32_e32 v219, v219, v159
	v_add_f32_e32 v219, v219, v161
	v_fma_f32 v219, v219, v229, -v161
	v_lshlrev_b32_e32 v124, 16, v49
	v_and_b32_e32 v125, 0xffff0000, v49
	v_lshlrev_b32_e32 v126, 16, v53
	v_and_b32_e32 v127, 0xffff0000, v53
	v_lshlrev_b32_e32 v128, 16, v57
	v_and_b32_e32 v129, 0xffff0000, v57
	v_lshlrev_b32_e32 v130, 16, v61
	v_and_b32_e32 v131, 0xffff0000, v61
	v_lshlrev_b32_e32 v132, 16, v65
	v_and_b32_e32 v133, 0xffff0000, v65
	v_lshlrev_b32_e32 v134, 16, v69
	v_and_b32_e32 v135, 0xffff0000, v69
	v_lshlrev_b32_e32 v136, 16, v73
	v_and_b32_e32 v137, 0xffff0000, v73
	v_lshlrev_b32_e32 v138, 16, v77
	v_and_b32_e32 v139, 0xffff0000, v77
	v_lshlrev_b32_e32 v140, 16, v81
	v_and_b32_e32 v141, 0xffff0000, v81
	v_lshlrev_b32_e32 v142, 16, v85
	v_and_b32_e32 v143, 0xffff0000, v85
	v_lshlrev_b32_e32 v144, 16, v89
	v_and_b32_e32 v145, 0xffff0000, v89
	v_lshlrev_b32_e32 v146, 16, v93
	v_and_b32_e32 v147, 0xffff0000, v93
	v_lshlrev_b32_e32 v148, 16, v97
	v_and_b32_e32 v149, 0xffff0000, v97
	v_lshlrev_b32_e32 v150, 16, v101
	v_and_b32_e32 v151, 0xffff0000, v101
	v_lshlrev_b32_e32 v152, 16, v105
	v_and_b32_e32 v153, 0xffff0000, v105
	v_lshlrev_b32_e32 v154, 16, v109
	v_and_b32_e32 v155, 0xffff0000, v109
	v_lshlrev_b32_e32 v156, 16, v113
	v_and_b32_e32 v157, 0xffff0000, v113
	v_lshlrev_b32_e32 v158, 16, v117
	v_and_b32_e32 v159, 0xffff0000, v117
	v_lshlrev_b32_e32 v160, 16, v121
	v_and_b32_e32 v161, 0xffff0000, v121
	v_add_f32_e32 v196, v124, v126
	v_add_f32_e32 v196, v196, v128
	v_add_f32_e32 v196, v196, v130
	v_add_f32_e32 v196, v196, v132
	v_add_f32_e32 v196, v196, v134
	v_add_f32_e32 v196, v196, v136
	v_add_f32_e32 v196, v196, v138
	v_add_f32_e32 v196, v196, v140
	v_add_f32_e32 v196, v196, v142
	v_add_f32_e32 v196, v196, v144
	v_add_f32_e32 v196, v196, v146
	v_add_f32_e32 v196, v196, v148
	v_add_f32_e32 v196, v196, v150
	v_add_f32_e32 v196, v196, v152
	v_add_f32_e32 v196, v196, v154
	v_fma_f32 v196, v196, v226, -v154
	v_add_f32_e32 v197, v125, v127
	v_add_f32_e32 v197, v197, v129
	v_add_f32_e32 v197, v197, v131
	v_add_f32_e32 v197, v197, v133
	v_add_f32_e32 v197, v197, v135
	v_add_f32_e32 v197, v197, v137
	v_add_f32_e32 v197, v197, v139
	v_add_f32_e32 v197, v197, v141
	v_add_f32_e32 v197, v197, v143
	v_add_f32_e32 v197, v197, v145
	v_add_f32_e32 v197, v197, v147
	v_add_f32_e32 v197, v197, v149
	v_add_f32_e32 v197, v197, v151
	v_add_f32_e32 v197, v197, v153
	v_add_f32_e32 v197, v197, v155
	v_fma_f32 v197, v197, v226, -v155
	v_add_f32_e32 v204, v126, v128
	v_add_f32_e32 v204, v204, v130
	v_add_f32_e32 v204, v204, v132
	v_add_f32_e32 v204, v204, v134
	v_add_f32_e32 v204, v204, v136
	v_add_f32_e32 v204, v204, v138
	v_add_f32_e32 v204, v204, v140
	v_add_f32_e32 v204, v204, v142
	v_add_f32_e32 v204, v204, v144
	v_add_f32_e32 v204, v204, v146
	v_add_f32_e32 v204, v204, v148
	v_add_f32_e32 v204, v204, v150
	v_add_f32_e32 v204, v204, v152
	v_add_f32_e32 v204, v204, v154
	v_add_f32_e32 v204, v204, v156
	v_fma_f32 v204, v204, v227, -v156
	v_add_f32_e32 v205, v127, v129
	v_add_f32_e32 v205, v205, v131
	v_add_f32_e32 v205, v205, v133
	v_add_f32_e32 v205, v205, v135
	v_add_f32_e32 v205, v205, v137
	v_add_f32_e32 v205, v205, v139
	v_add_f32_e32 v205, v205, v141
	v_add_f32_e32 v205, v205, v143
	v_add_f32_e32 v205, v205, v145
	v_add_f32_e32 v205, v205, v147
	v_add_f32_e32 v205, v205, v149
	v_add_f32_e32 v205, v205, v151
	v_add_f32_e32 v205, v205, v153
	v_add_f32_e32 v205, v205, v155
	v_add_f32_e32 v205, v205, v157
	v_fma_f32 v205, v205, v227, -v157
	v_add_f32_e32 v212, v128, v130
	v_add_f32_e32 v212, v212, v132
	v_add_f32_e32 v212, v212, v134
	v_add_f32_e32 v212, v212, v136
	v_add_f32_e32 v212, v212, v138
	v_add_f32_e32 v212, v212, v140
	v_add_f32_e32 v212, v212, v142
	v_add_f32_e32 v212, v212, v144
	v_add_f32_e32 v212, v212, v146
	v_add_f32_e32 v212, v212, v148
	v_add_f32_e32 v212, v212, v150
	v_add_f32_e32 v212, v212, v152
	v_add_f32_e32 v212, v212, v154
	v_add_f32_e32 v212, v212, v156
	v_add_f32_e32 v212, v212, v158
	v_fma_f32 v212, v212, v228, -v158
	v_add_f32_e32 v213, v129, v131
	v_add_f32_e32 v213, v213, v133
	v_add_f32_e32 v213, v213, v135
	v_add_f32_e32 v213, v213, v137
	v_add_f32_e32 v213, v213, v139
	v_add_f32_e32 v213, v213, v141
	v_add_f32_e32 v213, v213, v143
	v_add_f32_e32 v213, v213, v145
	v_add_f32_e32 v213, v213, v147
	v_add_f32_e32 v213, v213, v149
	v_add_f32_e32 v213, v213, v151
	v_add_f32_e32 v213, v213, v153
	v_add_f32_e32 v213, v213, v155
	v_add_f32_e32 v213, v213, v157
	v_add_f32_e32 v213, v213, v159
	v_fma_f32 v213, v213, v228, -v159
	v_add_f32_e32 v220, v130, v132
	v_add_f32_e32 v220, v220, v134
	v_add_f32_e32 v220, v220, v136
	v_add_f32_e32 v220, v220, v138
	v_add_f32_e32 v220, v220, v140
	v_add_f32_e32 v220, v220, v142
	v_add_f32_e32 v220, v220, v144
	v_add_f32_e32 v220, v220, v146
	v_add_f32_e32 v220, v220, v148
	v_add_f32_e32 v220, v220, v150
	v_add_f32_e32 v220, v220, v152
	v_add_f32_e32 v220, v220, v154
	v_add_f32_e32 v220, v220, v156
	v_add_f32_e32 v220, v220, v158
	v_add_f32_e32 v220, v220, v160
	v_fma_f32 v220, v220, v229, -v160
	v_add_f32_e32 v221, v131, v133
	v_add_f32_e32 v221, v221, v135
	v_add_f32_e32 v221, v221, v137
	v_add_f32_e32 v221, v221, v139
	v_add_f32_e32 v221, v221, v141
	v_add_f32_e32 v221, v221, v143
	v_add_f32_e32 v221, v221, v145
	v_add_f32_e32 v221, v221, v147
	v_add_f32_e32 v221, v221, v149
	v_add_f32_e32 v221, v221, v151
; __device__ __forceinline__ unsigned pk2(float lo, float hi) { return pg8::cvt_pk_bf16(lo, hi); }
; __device__ __forceinline__ void unpack8(const v4u w, float (&f)[8]) { f[0] = bflo(w.x); f[1] = bfhi(w.x); f[2] = bflo(w.y); f[3] = bfhi(w.y); f[4] = bflo(w.z); f[5] = bfhi(w.z); f[6] = bflo(w.w); f[7] = bfhi(w.w); }
; template <int W> __device__ __forceinline__ void pool_item(Frame& F, int row, int t, int c8) {
;     ...
;     for (int k = 0; k < W; ++k) { const int kk = (t - k) >= 0 ? k : t; ld[k] = *(const v4u*)(F.PROJ + (size_t)(row - kk) * INWP + O_UPOOL + c8); }
; #pragma unroll
;     for (int k = W - 1; k >= 0; --k) { unpack8(ld[k], u); const float wgt = (t - k) >= 0 ? 1.f : 0.f;
; #pragma unroll
;         for (int i = 0; i < 8; ++i) s[i] += wgt * u[i]; }
;     const int cnt = (t + 1) < W ? (t + 1) : W;
;     const float inv = 1.0f / (float)cnt;
;     v4u o; o.x = pk2(s[0] * inv - u[0], s[1] * inv - u[1]); o.y = pk2(s[2] * inv - u[2], s[3] * inv - u[3]); o.z = pk2(s[4] * inv - u[4], s[5] * inv - u[5]); o.w = pk2(s[6] * inv - u[6], s[7] * inv - u[7]);
	v_add_f32_e32 v221, v221, v153
	v_add_f32_e32 v221, v221, v155
	v_add_f32_e32 v221, v221, v157
	v_add_f32_e32 v221, v221, v159
	v_add_f32_e32 v221, v221, v161
	v_fma_f32 v221, v221, v229, -v161
	v_lshlrev_b32_e32 v124, 16, v50
	v_and_b32_e32 v125, 0xffff0000, v50
	v_lshlrev_b32_e32 v126, 16, v54
	v_and_b32_e32 v127, 0xffff0000, v54
	v_lshlrev_b32_e32 v128, 16, v58
	v_and_b32_e32 v129, 0xffff0000, v58
	v_lshlrev_b32_e32 v130, 16, v62
	v_and_b32_e32 v131, 0xffff0000, v62
	v_lshlrev_b32_e32 v132, 16, v66
	v_and_b32_e32 v133, 0xffff0000, v66
	v_lshlrev_b32_e32 v134, 16, v70
	v_and_b32_e32 v135, 0xffff0000, v70
	v_lshlrev_b32_e32 v136, 16, v74
	v_and_b32_e32 v137, 0xffff0000, v74
	v_lshlrev_b32_e32 v138, 16, v78
	v_and_b32_e32 v139, 0xffff0000, v78
	v_lshlrev_b32_e32 v140, 16, v82
	v_and_b32_e32 v141, 0xffff0000, v82
	v_lshlrev_b32_e32 v142, 16, v86
	v_and_b32_e32 v143, 0xffff0000, v86
	v_lshlrev_b32_e32 v144, 16, v90
	v_and_b32_e32 v145, 0xffff0000, v90
	v_lshlrev_b32_e32 v146, 16, v94
	v_and_b32_e32 v147, 0xffff0000, v94
	v_lshlrev_b32_e32 v148, 16, v98
	v_and_b32_e32 v149, 0xffff0000, v98
	v_lshlrev_b32_e32 v150, 16, v102
	v_and_b32_e32 v151, 0xffff0000, v102
	v_lshlrev_b32_e32 v152, 16, v106
	v_and_b32_e32 v153, 0xffff0000, v106
	v_lshlrev_b32_e32 v154, 16, v110
	v_and_b32_e32 v155, 0xffff0000, v110
	v_lshlrev_b32_e32 v156, 16, v114
	v_and_b32_e32 v157, 0xffff0000, v114
	v_lshlrev_b32_e32 v158, 16, v118
	v_and_b32_e32 v159, 0xffff0000, v118
	v_lshlrev_b32_e32 v160, 16, v122
	v_and_b32_e32 v161, 0xffff0000, v122
	v_add_f32_e32 v198, v124, v126
	v_add_f32_e32 v198, v198, v128
	v_add_f32_e32 v198, v198, v130
	v_add_f32_e32 v198, v198, v132
	v_add_f32_e32 v198, v198, v134
	v_add_f32_e32 v198, v198, v136
	v_add_f32_e32 v198, v198, v138
	v_add_f32_e32 v198, v198, v140
	v_add_f32_e32 v198, v198, v142
	v_add_f32_e32 v198, v198, v144
	v_add_f32_e32 v198, v198, v146
	v_add_f32_e32 v198, v198, v148
	v_add_f32_e32 v198, v198, v150
	v_add_f32_e32 v198, v198, v152
	v_add_f32_e32 v198, v198, v154
	v_fma_f32 v198, v198, v226, -v154
	v_add_f32_e32 v199, v125, v127
	v_add_f32_e32 v199, v199, v129
	v_add_f32_e32 v199, v199, v131
	v_add_f32_e32 v199, v199, v133
	v_add_f32_e32 v199, v199, v135
	v_add_f32_e32 v199, v199, v137
	v_add_f32_e32 v199, v199, v139
	v_add_f32_e32 v199, v199, v141
	v_add_f32_e32 v199, v199, v143
	v_add_f32_e32 v199, v199, v145
	v_add_f32_e32 v199, v199, v147
	v_add_f32_e32 v199, v199, v149
	v_add_f32_e32 v199, v199, v151
	v_add_f32_e32 v199, v199, v153
	v_add_f32_e32 v199, v199, v155
	v_fma_f32 v199, v199, v226, -v155
	v_add_f32_e32 v206, v126, v128
	v_add_f32_e32 v206, v206, v130
	v_add_f32_e32 v206, v206, v132
	v_add_f32_e32 v206, v206, v134
	v_add_f32_e32 v206, v206, v136
	v_add_f32_e32 v206, v206, v138
	v_add_f32_e32 v206, v206, v140
	v_add_f32_e32 v206, v206, v142
	v_add_f32_e32 v206, v206, v144
	v_add_f32_e32 v206, v206, v146
	v_add_f32_e32 v206, v206, v148
	v_add_f32_e32 v206, v206, v150
	v_add_f32_e32 v206, v206, v152
	v_add_f32_e32 v206, v206, v154
	v_add_f32_e32 v206, v206, v156
	v_fma_f32 v206, v206, v227, -v156
	v_add_f32_e32 v207, v127, v129
	v_add_f32_e32 v207, v207, v131
	v_add_f32_e32 v207, v207, v133
	v_add_f32_e32 v207, v207, v135
	v_add_f32_e32 v207, v207, v137
	v_add_f32_e32 v207, v207, v139
	v_add_f32_e32 v207, v207, v141
	v_add_f32_e32 v207, v207, v143
	v_add_f32_e32 v207, v207, v145
	v_add_f32_e32 v207, v207, v147
	v_add_f32_e32 v207, v207, v149
	v_add_f32_e32 v207, v207, v151
	v_add_f32_e32 v207, v207, v153
	v_add_f32_e32 v207, v207, v155
	v_add_f32_e32 v207, v207, v157
	v_fma_f32 v207, v207, v227, -v157
	v_add_f32_e32 v214, v128, v130
	v_add_f32_e32 v214, v214, v132
	v_add_f32_e32 v214, v214, v134
	v_add_f32_e32 v214, v214, v136
	v_add_f32_e32 v214, v214, v138
	v_add_f32_e32 v214, v214, v140
	v_add_f32_e32 v214, v214, v142
	v_add_f32_e32 v214, v214, v144
	v_add_f32_e32 v214, v214, v146
	v_add_f32_e32 v214, v214, v148
	v_add_f32_e32 v214, v214, v150
	v_add_f32_e32 v214, v214, v152
	v_add_f32_e32 v214, v214, v154
	v_add_f32_e32 v214, v214, v156
	v_add_f32_e32 v214, v214, v158
	v_fma_f32 v214, v214, v228, -v158
	v_add_f32_e32 v215, v129, v131
	v_add_f32_e32 v215, v215, v133
	v_add_f32_e32 v215, v215, v135
	v_add_f32_e32 v215, v215, v137
	v_add_f32_e32 v215, v215, v139
	v_add_f32_e32 v215, v215, v141
	v_add_f32_e32 v215, v215, v143
	v_add_f32_e32 v215, v215, v145
	v_add_f32_e32 v215, v215, v147
	v_add_f32_e32 v215, v215, v149
	v_add_f32_e32 v215, v215, v151
	v_add_f32_e32 v215, v215, v153
	v_add_f32_e32 v215, v215, v155
	v_add_f32_e32 v215, v215, v157
	v_add_f32_e32 v215, v215, v159
	v_fma_f32 v215, v215, v228, -v159
	v_add_f32_e32 v222, v130, v132
	v_add_f32_e32 v222, v222, v134
	v_add_f32_e32 v222, v222, v136
	v_add_f32_e32 v222, v222, v138
	v_add_f32_e32 v222, v222, v140
	v_add_f32_e32 v222, v222, v142
	v_add_f32_e32 v222, v222, v144
	v_add_f32_e32 v222, v222, v146
	v_add_f32_e32 v222, v222, v148
	v_add_f32_e32 v222, v222, v150
	v_add_f32_e32 v222, v222, v152
	v_add_f32_e32 v222, v222, v154
	v_add_f32_e32 v222, v222, v156
	v_add_f32_e32 v222, v222, v158
	v_add_f32_e32 v222, v222, v160
	v_fma_f32 v222, v222, v229, -v160
	v_add_f32_e32 v223, v131, v133
	v_add_f32_e32 v223, v223, v135
	v_add_f32_e32 v223, v223, v137
	v_add_f32_e32 v223, v223, v139
	v_add_f32_e32 v223, v223, v141
	v_add_f32_e32 v223, v223, v143
	v_add_f32_e32 v223, v223, v145
	v_add_f32_e32 v223, v223, v147
	v_add_f32_e32 v223, v223, v149
	v_add_f32_e32 v223, v223, v151
	v_add_f32_e32 v223, v223, v153
	v_add_f32_e32 v223, v223, v155
	v_add_f32_e32 v223, v223, v157
	v_add_f32_e32 v223, v223, v159
	v_add_f32_e32 v223, v223, v161
	v_fma_f32 v223, v223, v229, -v161
; __device__ __forceinline__ unsigned pk2(float lo, float hi) { return pg8::cvt_pk_bf16(lo, hi); }
; __device__ __forceinline__ void unpack8(const v4u w, float (&f)[8]) { f[0] = bflo(w.x); f[1] = bfhi(w.x); f[2] = bflo(w.y); f[3] = bfhi(w.y); f[4] = bflo(w.z); f[5] = bfhi(w.z); f[6] = bflo(w.w); f[7] = bfhi(w.w); }
; template <int W> __device__ __forceinline__ void pool_item(Frame& F, int row, int t, int c8) {
;     ...
;     for (int k = 0; k < W; ++k) { const int kk = (t - k) >= 0 ? k : t; ld[k] = *(const v4u*)(F.PROJ + (size_t)(row - kk) * INWP + O_UPOOL + c8); }
; #pragma unroll
;     for (int k = W - 1; k >= 0; --k) { unpack8(ld[k], u); const float wgt = (t - k) >= 0 ? 1.f : 0.f;
; #pragma unroll
;         for (int i = 0; i < 8; ++i) s[i] += wgt * u[i]; }
;     const int cnt = (t + 1) < W ? (t + 1) : W;
;     const float inv = 1.0f / (float)cnt;
;     v4u o; o.x = pk2(s[0] * inv - u[0], s[1] * inv - u[1]); o.y = pk2(s[2] * inv - u[2], s[3] * inv - u[3]); o.z = pk2(s[4] * inv - u[4], s[5] * inv - u[5]); o.w = pk2(s[6] * inv - u[6], s[7] * inv - u[7]);
;     *(v4u*)(F.Y + (size_t)row * 1024 + c8) = o;
	v_lshlrev_b32_e32 v124, 16, v51
	v_and_b32_e32 v125, 0xffff0000, v51
	v_lshlrev_b32_e32 v126, 16, v55
	v_and_b32_e32 v127, 0xffff0000, v55
	v_lshlrev_b32_e32 v128, 16, v59
	v_and_b32_e32 v129, 0xffff0000, v59
	v_lshlrev_b32_e32 v130, 16, v63
	v_and_b32_e32 v131, 0xffff0000, v63
	v_lshlrev_b32_e32 v132, 16, v67
	v_and_b32_e32 v133, 0xffff0000, v67
	v_lshlrev_b32_e32 v134, 16, v71
	v_and_b32_e32 v135, 0xffff0000, v71
	v_lshlrev_b32_e32 v136, 16, v75
	v_and_b32_e32 v137, 0xffff0000, v75
	v_lshlrev_b32_e32 v138, 16, v79
	v_and_b32_e32 v139, 0xffff0000, v79
	v_lshlrev_b32_e32 v140, 16, v83
	v_and_b32_e32 v141, 0xffff0000, v83
	v_lshlrev_b32_e32 v142, 16, v87
	v_and_b32_e32 v143, 0xffff0000, v87
	v_lshlrev_b32_e32 v144, 16, v91
	v_and_b32_e32 v145, 0xffff0000, v91
	v_lshlrev_b32_e32 v146, 16, v95
	v_and_b32_e32 v147, 0xffff0000, v95
	v_lshlrev_b32_e32 v148, 16, v99
	v_and_b32_e32 v149, 0xffff0000, v99
	v_lshlrev_b32_e32 v150, 16, v103
	v_and_b32_e32 v151, 0xffff0000, v103
	v_lshlrev_b32_e32 v152, 16, v107
	v_and_b32_e32 v153, 0xffff0000, v107
	v_lshlrev_b32_e32 v154, 16, v111
	v_and_b32_e32 v155, 0xffff0000, v111
	v_lshlrev_b32_e32 v156, 16, v115
	v_and_b32_e32 v157, 0xffff0000, v115
	v_lshlrev_b32_e32 v158, 16, v119
	v_and_b32_e32 v159, 0xffff0000, v119
	v_lshlrev_b32_e32 v160, 16, v123
	v_and_b32_e32 v161, 0xffff0000, v123
	v_add_f32_e32 v200, v124, v126
	v_add_f32_e32 v200, v200, v128
	v_add_f32_e32 v200, v200, v130
	v_add_f32_e32 v200, v200, v132
	v_add_f32_e32 v200, v200, v134
	v_add_f32_e32 v200, v200, v136
	v_add_f32_e32 v200, v200, v138
	v_add_f32_e32 v200, v200, v140
	v_add_f32_e32 v200, v200, v142
	v_add_f32_e32 v200, v200, v144
	v_add_f32_e32 v200, v200, v146
	v_add_f32_e32 v200, v200, v148
	v_add_f32_e32 v200, v200, v150
	v_add_f32_e32 v200, v200, v152
	v_add_f32_e32 v200, v200, v154
	v_fma_f32 v200, v200, v226, -v154
	v_add_f32_e32 v201, v125, v127
	v_add_f32_e32 v201, v201, v129
	v_add_f32_e32 v201, v201, v131
	v_add_f32_e32 v201, v201, v133
	v_add_f32_e32 v201, v201, v135
	v_add_f32_e32 v201, v201, v137
	v_add_f32_e32 v201, v201, v139
	v_add_f32_e32 v201, v201, v141
	v_add_f32_e32 v201, v201, v143
	v_add_f32_e32 v201, v201, v145
	v_add_f32_e32 v201, v201, v147
	v_add_f32_e32 v201, v201, v149
	v_add_f32_e32 v201, v201, v151
	v_add_f32_e32 v201, v201, v153
	v_add_f32_e32 v201, v201, v155
	v_fma_f32 v201, v201, v226, -v155
	v_add_f32_e32 v208, v126, v128
	v_add_f32_e32 v208, v208, v130
	v_add_f32_e32 v208, v208, v132
	v_add_f32_e32 v208, v208, v134
	v_add_f32_e32 v208, v208, v136
	v_add_f32_e32 v208, v208, v138
	v_add_f32_e32 v208, v208, v140
	v_add_f32_e32 v208, v208, v142
	v_add_f32_e32 v208, v208, v144
	v_add_f32_e32 v208, v208, v146
	v_add_f32_e32 v208, v208, v148
	v_add_f32_e32 v208, v208, v150
	v_add_f32_e32 v208, v208, v152
	v_add_f32_e32 v208, v208, v154
	v_add_f32_e32 v208, v208, v156
	v_fma_f32 v208, v208, v227, -v156
	v_add_f32_e32 v209, v127, v129
	v_add_f32_e32 v209, v209, v131
	v_add_f32_e32 v209, v209, v133
	v_add_f32_e32 v209, v209, v135
	v_add_f32_e32 v209, v209, v137
	v_add_f32_e32 v209, v209, v139
	v_add_f32_e32 v209, v209, v141
	v_add_f32_e32 v209, v209, v143
	v_add_f32_e32 v209, v209, v145
	v_add_f32_e32 v209, v209, v147
	v_add_f32_e32 v209, v209, v149
	v_add_f32_e32 v209, v209, v151
	v_add_f32_e32 v209, v209, v153
	v_add_f32_e32 v209, v209, v155
	v_add_f32_e32 v209, v209, v157
	v_fma_f32 v209, v209, v227, -v157
	v_add_f32_e32 v216, v128, v130
	v_add_f32_e32 v216, v216, v132
	v_add_f32_e32 v216, v216, v134
	v_add_f32_e32 v216, v216, v136
	v_add_f32_e32 v216, v216, v138
	v_add_f32_e32 v216, v216, v140
	v_add_f32_e32 v216, v216, v142
	v_add_f32_e32 v216, v216, v144
	v_add_f32_e32 v216, v216, v146
	v_add_f32_e32 v216, v216, v148
	v_add_f32_e32 v216, v216, v150
	v_add_f32_e32 v216, v216, v152
	v_add_f32_e32 v216, v216, v154
	v_add_f32_e32 v216, v216, v156
	v_add_f32_e32 v216, v216, v158
	v_fma_f32 v216, v216, v228, -v158
	v_add_f32_e32 v217, v129, v131
	v_add_f32_e32 v217, v217, v133
	v_add_f32_e32 v217, v217, v135
	v_add_f32_e32 v217, v217, v137
	v_add_f32_e32 v217, v217, v139
	v_add_f32_e32 v217, v217, v141
	v_add_f32_e32 v217, v217, v143
	v_add_f32_e32 v217, v217, v145
	v_add_f32_e32 v217, v217, v147
	v_add_f32_e32 v217, v217, v149
	v_add_f32_e32 v217, v217, v151
	v_add_f32_e32 v217, v217, v153
	v_add_f32_e32 v217, v217, v155
	v_add_f32_e32 v217, v217, v157
	v_add_f32_e32 v217, v217, v159
	v_fma_f32 v217, v217, v228, -v159
	v_add_f32_e32 v224, v130, v132
	v_add_f32_e32 v224, v224, v134
	v_add_f32_e32 v224, v224, v136
	v_add_f32_e32 v224, v224, v138
	v_add_f32_e32 v224, v224, v140
	v_add_f32_e32 v224, v224, v142
	v_add_f32_e32 v224, v224, v144
	v_add_f32_e32 v224, v224, v146
	v_add_f32_e32 v224, v224, v148
	v_add_f32_e32 v224, v224, v150
	v_add_f32_e32 v224, v224, v152
	v_add_f32_e32 v224, v224, v154
	v_add_f32_e32 v224, v224, v156
	v_add_f32_e32 v224, v224, v158
	v_add_f32_e32 v224, v224, v160
	v_fma_f32 v224, v224, v229, -v160
	v_add_f32_e32 v225, v131, v133
	v_add_f32_e32 v225, v225, v135
	v_add_f32_e32 v225, v225, v137
	v_add_f32_e32 v225, v225, v139
	v_add_f32_e32 v225, v225, v141
	v_add_f32_e32 v225, v225, v143
	v_add_f32_e32 v225, v225, v145
	v_add_f32_e32 v225, v225, v147
	v_add_f32_e32 v225, v225, v149
	v_add_f32_e32 v225, v225, v151
	v_add_f32_e32 v225, v225, v153
	v_add_f32_e32 v225, v225, v155
	v_add_f32_e32 v225, v225, v157
	v_add_f32_e32 v225, v225, v159
	v_add_f32_e32 v225, v225, v161
	v_fma_f32 v225, v225, v229, -v161
	v_cvt_pk_bf16_f32 v194, v194, v195
	v_cvt_pk_bf16_f32 v195, v196, v197
	v_cvt_pk_bf16_f32 v196, v198, v199
	v_cvt_pk_bf16_f32 v197, v200, v201
	global_store_dwordx4 v17, v[194:197], s[14:15]
	v_cvt_pk_bf16_f32 v202, v202, v203
	v_cvt_pk_bf16_f32 v203, v204, v205
	v_cvt_pk_bf16_f32 v204, v206, v207
	v_cvt_pk_bf16_f32 v205, v208, v209
	v_add_u32_e32 v13, 0x800, v17
	global_store_dwordx4 v13, v[202:205], s[14:15]
	v_cvt_pk_bf16_f32 v210, v210, v211
	v_cvt_pk_bf16_f32 v211, v212, v213
	v_cvt_pk_bf16_f32 v212, v214, v215
	v_cvt_pk_bf16_f32 v213, v216, v217
	v_add_u32_e32 v13, 0x1000, v17
	global_store_dwordx4 v13, v[210:213], s[14:15]
	v_cvt_pk_bf16_f32 v218, v218, v219
	v_cvt_pk_bf16_f32 v219, v220, v221
	v_cvt_pk_bf16_f32 v220, v222, v223
	v_cvt_pk_bf16_f32 v221, v224, v225
	v_add_u32_e32 v13, 0x1800, v17
	global_store_dwordx4 v13, v[218:221], s[14:15]
	s_branch .Lpc_conv
; __device__ __forceinline__ unsigned pk2(float lo, float hi) { return pg8::cvt_pk_bf16(lo, hi); }
; __device__ __forceinline__ void unpack8(const v4u w, float (&f)[8]) { f[0] = bflo(w.x); f[1] = bfhi(w.x); f[2] = bflo(w.y); f[3] = bfhi(w.y); f[4] = bflo(w.z); f[5] = bfhi(w.z); f[6] = bflo(w.w); f[7] = bfhi(w.w); }
; __device__ __forceinline__ int lane_id() { int l; asm volatile("s_nop 4\n\tv_mbcnt_lo_u32_b32 %0, -1, 0\n\tv_mbcnt_hi_u32_b32 %0, -1, %0\n\ts_nop 4" : "=v"(l)); return l; }
; template <int W> __device__ __forceinline__ void pool_item(Frame& F, int row, int t, int c8) {
;     float s[8], u[8];
; #pragma unroll
;     for (int i = 0; i < 8; ++i) s[i] = 0.f;
;     v4u ld[W];
; #pragma unroll
;     for (int k = 0; k < W; ++k) { const int kk = (t - k) >= 0 ? k : t; ld[k] = *(const v4u*)(F.PROJ + (size_t)(row - kk) * INWP + O_UPOOL + c8); }
; #pragma unroll
;     for (int k = W - 1; k >= 0; --k) { unpack8(ld[k], u); const float wgt = (t - k) >= 0 ? 1.f : 0.f;
; #pragma unroll
;         for (int i = 0; i < 8; ++i) s[i] += wgt * u[i]; }
;     const int cnt = (t + 1) < W ? (t + 1) : W;
;     const float inv = 1.0f / (float)cnt;
;     v4u o; o.x = pk2(s[0] * inv - u[0], s[1] * inv - u[1]); o.y = pk2(s[2] * inv - u[2], s[3] * inv - u[3]); o.z = pk2(s[4] * inv - u[4], s[5] * inv - u[5]); o.w = pk2(s[6] * inv - u[6], s[7] * inv - u[7]);
;     *(v4u*)(F.Y + (size_t)row * 1024 + c8) = o;
; }
; __device__ __forceinline__ void poolconv_phase(Frame& F, const float* conv_w_l) {
;     int tid = F.wave * 64 + lane_id(); asm volatile("" : "+v"(tid));
;     const int gt = F.vcu * NTHR + tid, NGT = F.G * NTHR;
;     for (int idx = gt; idx < M * 128; idx += NGT) {
;         const int grp = idx / (M * 32), rem = idx - grp * (M * 32), row = rem >> 5, c8 = grp * 256 + (rem & 31) * 8, t = row & (SEQ - 1);
;         if (grp == 0) pool_item<2>(F, row, t, c8); else if (grp == 1) pool_item<4>(F, row, t, c8); else if (grp == 2) pool_item<8>(F, row, t, c8); else pool_item<16>(F, row, t, c8);
;     }
.Lpc_g1:
	v_add_u32_e32 v14, 0x200, v7
	v_add_u32_e32 v15, 0x400, v7
	v_add_u32_e32 v16, 0x200, v9
	v_add_u32_e32 v17, 0x400, v9
	v_min_u32_e32 v11, 0xa200, v6
	v_sub_u32_e32 v12, v14, v11
	global_load_dwordx4 v[20:23], v12, s[96:97] nt
	v_min_u32_e32 v11, 0x6c00, v6
	v_sub_u32_e32 v12, v14, v11
	global_load_dwordx4 v[24:27], v12, s[96:97] nt
	v_min_u32_e32 v11, 0x3600, v6
	v_sub_u32_e32 v12, v14, v11
	global_load_dwordx4 v[28:31], v12, s[96:97] nt
	global_load_dwordx4 v[32:35], v14, s[96:97] nt
	v_add_u32_e32 v12, 0x3600, v14
	global_load_dwordx4 v[36:39], v12, s[96:97] nt
	v_add_u32_e32 v12, 0x6c00, v14
	global_load_dwordx4 v[40:43], v12, s[96:97] nt
	v_add_u32_e32 v12, 0xa200, v14
	global_load_dwordx4 v[44:47], v12, s[96:97] nt
	v_min_u32_e32 v11, 0x17a00, v6
	v_sub_u32_e32 v12, v15, v11
	global_load_dwordx4 v[48:51], v12, s[96:97] nt
	v_min_u32_e32 v11, 0x14400, v6
	v_sub_u32_e32 v12, v15, v11
	global_load_dwordx4 v[52:55], v12, s[96:97] nt
	v_min_u32_e32 v11, 0x10e00, v6
	v_sub_u32_e32 v12, v15, v11
	global_load_dwordx4 v[56:59], v12, s[96:97] nt
	v_min_u32_e32 v11, 0xd800, v6
	v_sub_u32_e32 v12, v15, v11
	global_load_dwordx4 v[60:63], v12, s[96:97] nt
	v_min_u32_e32 v11, 0xa200, v6
	v_sub_u32_e32 v12, v15, v11
	global_load_dwordx4 v[64:67], v12, s[96:97] nt
	v_min_u32_e32 v11, 0x6c00, v6
	v_sub_u32_e32 v12, v15, v11
	global_load_dwordx4 v[68:71], v12, s[96:97] nt
	v_min_u32_e32 v11, 0x3600, v6
	v_sub_u32_e32 v12, v15, v11
	global_load_dwordx4 v[72:75], v12, s[96:97] nt
	global_load_dwordx4 v[76:79], v15, s[96:97] nt
	v_add_u32_e32 v12, 0x3600, v15
	global_load_dwordx4 v[80:83], v12, s[96:97] nt
	v_add_u32_e32 v12, 0x6c00, v15
	global_load_dwordx4 v[84:87], v12, s[96:97] nt
	v_add_u32_e32 v12, 0xa200, v15
	global_load_dwordx4 v[88:91], v12, s[96:97] nt
	s_waitcnt vmcnt(11)
	v_cmp_le_u32_e32 vcc, 3, v5
	s_nop 1
	v_cndmask_b32_e32 v20, 0, v20, vcc
	v_cndmask_b32_e32 v21, 0, v21, vcc
	v_cndmask_b32_e32 v22, 0, v22, vcc
	v_cndmask_b32_e32 v23, 0, v23, vcc
	v_cmp_le_u32_e32 vcc, 2, v5
	s_nop 1
	v_cndmask_b32_e32 v24, 0, v24, vcc
	v_cndmask_b32_e32 v25, 0, v25, vcc
	v_cndmask_b32_e32 v26, 0, v26, vcc
	v_cndmask_b32_e32 v27, 0, v27, vcc
	v_cmp_le_u32_e32 vcc, 1, v5
	s_nop 1
	v_cndmask_b32_e32 v28, 0, v28, vcc
	v_cndmask_b32_e32 v29, 0, v29, vcc
	v_cndmask_b32_e32 v30, 0, v30, vcc
	v_cndmask_b32_e32 v31, 0, v31, vcc
	v_add_u32_e32 v226, 1, v5
	v_min_u32_e32 v226, 4, v226
	v_cvt_f32_u32_e32 v226, v226
	v_rcp_f32_e32 v226, v226
	v_add_u32_e32 v227, 2, v5
	v_min_u32_e32 v227, 4, v227
	v_cvt_f32_u32_e32 v227, v227
	v_rcp_f32_e32 v227, v227
	v_add_u32_e32 v228, 3, v5
	v_min_u32_e32 v228, 4, v228
	v_cvt_f32_u32_e32 v228, v228
	v_rcp_f32_e32 v228, v228
	v_add_u32_e32 v229, 4, v5
	v_min_u32_e32 v229, 4, v229
	v_cvt_f32_u32_e32 v229, v229
	v_rcp_f32_e32 v229, v229
	v_lshlrev_b32_e32 v124, 16, v20
	v_and_b32_e32 v125, 0xffff0000, v20
	v_lshlrev_b32_e32 v126, 16, v24
	v_and_b32_e32 v127, 0xffff0000, v24
	v_lshlrev_b32_e32 v128, 16, v28
	v_and_b32_e32 v129, 0xffff0000, v28
	v_lshlrev_b32_e32 v130, 16, v32
	v_and_b32_e32 v131, 0xffff0000, v32
	v_lshlrev_b32_e32 v132, 16, v36
	v_and_b32_e32 v133, 0xffff0000, v36
	v_lshlrev_b32_e32 v134, 16, v40
	v_and_b32_e32 v135, 0xffff0000, v40
	v_lshlrev_b32_e32 v136, 16, v44
	v_and_b32_e32 v137, 0xffff0000, v44
	v_add_f32_e32 v194, v124, v126
	v_add_f32_e32 v194, v194, v128
	v_add_f32_e32 v194, v194, v130
	v_fma_f32 v194, v194, v226, -v130
	v_add_f32_e32 v195, v125, v127
	v_add_f32_e32 v195, v195, v129
	v_add_f32_e32 v195, v195, v131
	v_fma_f32 v195, v195, v226, -v131
	v_add_f32_e32 v202, v126, v128
	v_add_f32_e32 v202, v202, v130
	v_add_f32_e32 v202, v202, v132
	v_fma_f32 v202, v202, v227, -v132
	v_add_f32_e32 v203, v127, v129
	v_add_f32_e32 v203, v203, v131
	v_add_f32_e32 v203, v203, v133
	v_fma_f32 v203, v203, v227, -v133
	v_add_f32_e32 v210, v128, v130
	v_add_f32_e32 v210, v210, v132
	v_add_f32_e32 v210, v210, v134
	v_fma_f32 v210, v210, v228, -v134
	v_add_f32_e32 v211, v129, v131
	v_add_f32_e32 v211, v211, v133
	v_add_f32_e32 v211, v211, v135
	v_fma_f32 v211, v211, v228, -v135
	v_add_f32_e32 v218, v130, v132
	v_add_f32_e32 v218, v218, v134
	v_add_f32_e32 v218, v218, v136
	v_fma_f32 v218, v218, v229, -v136
	v_add_f32_e32 v219, v131, v133
	v_add_f32_e32 v219, v219, v135
	v_add_f32_e32 v219, v219, v137
	v_fma_f32 v219, v219, v229, -v137
	v_lshlrev_b32_e32 v124, 16, v21
	v_and_b32_e32 v125, 0xffff0000, v21
	v_lshlrev_b32_e32 v126, 16, v25
	v_and_b32_e32 v127, 0xffff0000, v25
	v_lshlrev_b32_e32 v128, 16, v29
	v_and_b32_e32 v129, 0xffff0000, v29
	v_lshlrev_b32_e32 v130, 16, v33
	v_and_b32_e32 v131, 0xffff0000, v33
	v_lshlrev_b32_e32 v132, 16, v37
	v_and_b32_e32 v133, 0xffff0000, v37
	v_lshlrev_b32_e32 v134, 16, v41
	v_and_b32_e32 v135, 0xffff0000, v41
	v_lshlrev_b32_e32 v136, 16, v45
	v_and_b32_e32 v137, 0xffff0000, v45
	v_add_f32_e32 v196, v124, v126
	v_add_f32_e32 v196, v196, v128
	v_add_f32_e32 v196, v196, v130
	v_fma_f32 v196, v196, v226, -v130
	v_add_f32_e32 v197, v125, v127
	v_add_f32_e32 v197, v197, v129
	v_add_f32_e32 v197, v197, v131
	v_fma_f32 v197, v197, v226, -v131
	v_add_f32_e32 v204, v126, v128
	v_add_f32_e32 v204, v204, v130
	v_add_f32_e32 v204, v204, v132
	v_fma_f32 v204, v204, v227, -v132
	v_add_f32_e32 v205, v127, v129
	v_add_f32_e32 v205, v205, v131
	v_add_f32_e32 v205, v205, v133
	v_fma_f32 v205, v205, v227, -v133
	v_add_f32_e32 v212, v128, v130
	v_add_f32_e32 v212, v212, v132
	v_add_f32_e32 v212, v212, v134
	v_fma_f32 v212, v212, v228, -v134
	v_add_f32_e32 v213, v129, v131
	v_add_f32_e32 v213, v213, v133
	v_add_f32_e32 v213, v213, v135
	v_fma_f32 v213, v213, v228, -v135
	v_add_f32_e32 v220, v130, v132
; __device__ __forceinline__ unsigned pk2(float lo, float hi) { return pg8::cvt_pk_bf16(lo, hi); }
; __device__ __forceinline__ void unpack8(const v4u w, float (&f)[8]) { f[0] = bflo(w.x); f[1] = bfhi(w.x); f[2] = bflo(w.y); f[3] = bfhi(w.y); f[4] = bflo(w.z); f[5] = bfhi(w.z); f[6] = bflo(w.w); f[7] = bfhi(w.w); }
; template <int W> __device__ __forceinline__ void pool_item(Frame& F, int row, int t, int c8) {
;     ...
;     for (int k = 0; k < W; ++k) { const int kk = (t - k) >= 0 ? k : t; ld[k] = *(const v4u*)(F.PROJ + (size_t)(row - kk) * INWP + O_UPOOL + c8); }
; #pragma unroll
;     for (int k = W - 1; k >= 0; --k) { unpack8(ld[k], u); const float wgt = (t - k) >= 0 ? 1.f : 0.f;
; #pragma unroll
;         for (int i = 0; i < 8; ++i) s[i] += wgt * u[i]; }
;     const int cnt = (t + 1) < W ? (t + 1) : W;
;     const float inv = 1.0f / (float)cnt;
;     v4u o; o.x = pk2(s[0] * inv - u[0], s[1] * inv - u[1]); o.y = pk2(s[2] * inv - u[2], s[3] * inv - u[3]); o.z = pk2(s[4] * inv - u[4], s[5] * inv - u[5]); o.w = pk2(s[6] * inv - u[6], s[7] * inv - u[7]);
;     *(v4u*)(F.Y + (size_t)row * 1024 + c8) = o;
	v_add_f32_e32 v220, v220, v134
	v_add_f32_e32 v220, v220, v136
	v_fma_f32 v220, v220, v229, -v136
	v_add_f32_e32 v221, v131, v133
	v_add_f32_e32 v221, v221, v135
	v_add_f32_e32 v221, v221, v137
	v_fma_f32 v221, v221, v229, -v137
	v_lshlrev_b32_e32 v124, 16, v22
	v_and_b32_e32 v125, 0xffff0000, v22
	v_lshlrev_b32_e32 v126, 16, v26
	v_and_b32_e32 v127, 0xffff0000, v26
	v_lshlrev_b32_e32 v128, 16, v30
	v_and_b32_e32 v129, 0xffff0000, v30
	v_lshlrev_b32_e32 v130, 16, v34
	v_and_b32_e32 v131, 0xffff0000, v34
	v_lshlrev_b32_e32 v132, 16, v38
	v_and_b32_e32 v133, 0xffff0000, v38
	v_lshlrev_b32_e32 v134, 16, v42
	v_and_b32_e32 v135, 0xffff0000, v42
	v_lshlrev_b32_e32 v136, 16, v46
	v_and_b32_e32 v137, 0xffff0000, v46
	v_add_f32_e32 v198, v124, v126
	v_add_f32_e32 v198, v198, v128
	v_add_f32_e32 v198, v198, v130
	v_fma_f32 v198, v198, v226, -v130
	v_add_f32_e32 v199, v125, v127
	v_add_f32_e32 v199, v199, v129
	v_add_f32_e32 v199, v199, v131
	v_fma_f32 v199, v199, v226, -v131
	v_add_f32_e32 v206, v126, v128
	v_add_f32_e32 v206, v206, v130
	v_add_f32_e32 v206, v206, v132
	v_fma_f32 v206, v206, v227, -v132
	v_add_f32_e32 v207, v127, v129
	v_add_f32_e32 v207, v207, v131
	v_add_f32_e32 v207, v207, v133
	v_fma_f32 v207, v207, v227, -v133
	v_add_f32_e32 v214, v128, v130
	v_add_f32_e32 v214, v214, v132
	v_add_f32_e32 v214, v214, v134
	v_fma_f32 v214, v214, v228, -v134
	v_add_f32_e32 v215, v129, v131
	v_add_f32_e32 v215, v215, v133
	v_add_f32_e32 v215, v215, v135
	v_fma_f32 v215, v215, v228, -v135
	v_add_f32_e32 v222, v130, v132
	v_add_f32_e32 v222, v222, v134
	v_add_f32_e32 v222, v222, v136
	v_fma_f32 v222, v222, v229, -v136
	v_add_f32_e32 v223, v131, v133
	v_add_f32_e32 v223, v223, v135
	v_add_f32_e32 v223, v223, v137
	v_fma_f32 v223, v223, v229, -v137
	v_lshlrev_b32_e32 v124, 16, v23
	v_and_b32_e32 v125, 0xffff0000, v23
	v_lshlrev_b32_e32 v126, 16, v27
	v_and_b32_e32 v127, 0xffff0000, v27
	v_lshlrev_b32_e32 v128, 16, v31
	v_and_b32_e32 v129, 0xffff0000, v31
	v_lshlrev_b32_e32 v130, 16, v35
	v_and_b32_e32 v131, 0xffff0000, v35
	v_lshlrev_b32_e32 v132, 16, v39
	v_and_b32_e32 v133, 0xffff0000, v39
	v_lshlrev_b32_e32 v134, 16, v43
	v_and_b32_e32 v135, 0xffff0000, v43
	v_lshlrev_b32_e32 v136, 16, v47
	v_and_b32_e32 v137, 0xffff0000, v47
	v_add_f32_e32 v200, v124, v126
	v_add_f32_e32 v200, v200, v128
	v_add_f32_e32 v200, v200, v130
	v_fma_f32 v200, v200, v226, -v130
	v_add_f32_e32 v201, v125, v127
	v_add_f32_e32 v201, v201, v129
	v_add_f32_e32 v201, v201, v131
	v_fma_f32 v201, v201, v226, -v131
	v_add_f32_e32 v208, v126, v128
	v_add_f32_e32 v208, v208, v130
	v_add_f32_e32 v208, v208, v132
	v_fma_f32 v208, v208, v227, -v132
	v_add_f32_e32 v209, v127, v129
	v_add_f32_e32 v209, v209, v131
	v_add_f32_e32 v209, v209, v133
	v_fma_f32 v209, v209, v227, -v133
	v_add_f32_e32 v216, v128, v130
	v_add_f32_e32 v216, v216, v132
	v_add_f32_e32 v216, v216, v134
	v_fma_f32 v216, v216, v228, -v134
	v_add_f32_e32 v217, v129, v131
	v_add_f32_e32 v217, v217, v133
	v_add_f32_e32 v217, v217, v135
	v_fma_f32 v217, v217, v228, -v135
	v_add_f32_e32 v224, v130, v132
	v_add_f32_e32 v224, v224, v134
	v_add_f32_e32 v224, v224, v136
	v_fma_f32 v224, v224, v229, -v136
	v_add_f32_e32 v225, v131, v133
	v_add_f32_e32 v225, v225, v135
	v_add_f32_e32 v225, v225, v137
	v_fma_f32 v225, v225, v229, -v137
	v_cvt_pk_bf16_f32 v194, v194, v195
	v_cvt_pk_bf16_f32 v195, v196, v197
	v_cvt_pk_bf16_f32 v196, v198, v199
	v_cvt_pk_bf16_f32 v197, v200, v201
	global_store_dwordx4 v16, v[194:197], s[14:15]
	v_cvt_pk_bf16_f32 v202, v202, v203
	v_cvt_pk_bf16_f32 v203, v204, v205
	v_cvt_pk_bf16_f32 v204, v206, v207
	v_cvt_pk_bf16_f32 v205, v208, v209
	v_add_u32_e32 v13, 0x800, v16
	global_store_dwordx4 v13, v[202:205], s[14:15]
	v_cvt_pk_bf16_f32 v210, v210, v211
	v_cvt_pk_bf16_f32 v211, v212, v213
	v_cvt_pk_bf16_f32 v212, v214, v215
	v_cvt_pk_bf16_f32 v213, v216, v217
	v_add_u32_e32 v13, 0x1000, v16
	global_store_dwordx4 v13, v[210:213], s[14:15]
	v_cvt_pk_bf16_f32 v218, v218, v219
	v_cvt_pk_bf16_f32 v219, v220, v221
	v_cvt_pk_bf16_f32 v220, v222, v223
	v_cvt_pk_bf16_f32 v221, v224, v225
	v_add_u32_e32 v13, 0x1800, v16
	global_store_dwordx4 v13, v[218:221], s[14:15]
	s_waitcnt vmcnt(4)
	v_cmp_le_u32_e32 vcc, 7, v5
	s_nop 1
	v_cndmask_b32_e32 v48, 0, v48, vcc
	v_cndmask_b32_e32 v49, 0, v49, vcc
	v_cndmask_b32_e32 v50, 0, v50, vcc
	v_cndmask_b32_e32 v51, 0, v51, vcc
	v_cmp_le_u32_e32 vcc, 6, v5
	s_nop 1
	v_cndmask_b32_e32 v52, 0, v52, vcc
	v_cndmask_b32_e32 v53, 0, v53, vcc
	v_cndmask_b32_e32 v54, 0, v54, vcc
	v_cndmask_b32_e32 v55, 0, v55, vcc
	v_cmp_le_u32_e32 vcc, 5, v5
	s_nop 1
	v_cndmask_b32_e32 v56, 0, v56, vcc
	v_cndmask_b32_e32 v57, 0, v57, vcc
	v_cndmask_b32_e32 v58, 0, v58, vcc
	v_cndmask_b32_e32 v59, 0, v59, vcc
	v_cmp_le_u32_e32 vcc, 4, v5
	s_nop 1
	v_cndmask_b32_e32 v60, 0, v60, vcc
	v_cndmask_b32_e32 v61, 0, v61, vcc
	v_cndmask_b32_e32 v62, 0, v62, vcc
	v_cndmask_b32_e32 v63, 0, v63, vcc
	v_cmp_le_u32_e32 vcc, 3, v5
	s_nop 1
	v_cndmask_b32_e32 v64, 0, v64, vcc
	v_cndmask_b32_e32 v65, 0, v65, vcc
	v_cndmask_b32_e32 v66, 0, v66, vcc
	v_cndmask_b32_e32 v67, 0, v67, vcc
	v_cmp_le_u32_e32 vcc, 2, v5
	s_nop 1
	v_cndmask_b32_e32 v68, 0, v68, vcc
	v_cndmask_b32_e32 v69, 0, v69, vcc
	v_cndmask_b32_e32 v70, 0, v70, vcc
	v_cndmask_b32_e32 v71, 0, v71, vcc
	v_cmp_le_u32_e32 vcc, 1, v5
	s_nop 1
	v_cndmask_b32_e32 v72, 0, v72, vcc
	v_cndmask_b32_e32 v73, 0, v73, vcc
	v_cndmask_b32_e32 v74, 0, v74, vcc
	v_cndmask_b32_e32 v75, 0, v75, vcc
	v_add_u32_e32 v226, 1, v5
	v_min_u32_e32 v226, 8, v226
	v_cvt_f32_u32_e32 v226, v226
	v_rcp_f32_e32 v226, v226
	v_add_u32_e32 v227, 2, v5
	v_min_u32_e32 v227, 8, v227
; __device__ __forceinline__ unsigned pk2(float lo, float hi) { return pg8::cvt_pk_bf16(lo, hi); }
; __device__ __forceinline__ void unpack8(const v4u w, float (&f)[8]) { f[0] = bflo(w.x); f[1] = bfhi(w.x); f[2] = bflo(w.y); f[3] = bfhi(w.y); f[4] = bflo(w.z); f[5] = bfhi(w.z); f[6] = bflo(w.w); f[7] = bfhi(w.w); }
; template <int W> __device__ __forceinline__ void pool_item(Frame& F, int row, int t, int c8) {
;     ...
;     for (int k = 0; k < W; ++k) { const int kk = (t - k) >= 0 ? k : t; ld[k] = *(const v4u*)(F.PROJ + (size_t)(row - kk) * INWP + O_UPOOL + c8); }
; #pragma unroll
;     for (int k = W - 1; k >= 0; --k) { unpack8(ld[k], u); const float wgt = (t - k) >= 0 ? 1.f : 0.f;
; #pragma unroll
;         for (int i = 0; i < 8; ++i) s[i] += wgt * u[i]; }
;     const int cnt = (t + 1) < W ? (t + 1) : W;
;     const float inv = 1.0f / (float)cnt;
;     v4u o; o.x = pk2(s[0] * inv - u[0], s[1] * inv - u[1]); o.y = pk2(s[2] * inv - u[2], s[3] * inv - u[3]); o.z = pk2(s[4] * inv - u[4], s[5] * inv - u[5]); o.w = pk2(s[6] * inv - u[6], s[7] * inv - u[7]);
	v_cvt_f32_u32_e32 v227, v227
	v_rcp_f32_e32 v227, v227
	v_add_u32_e32 v228, 3, v5
	v_min_u32_e32 v228, 8, v228
	v_cvt_f32_u32_e32 v228, v228
	v_rcp_f32_e32 v228, v228
	v_add_u32_e32 v229, 4, v5
	v_min_u32_e32 v229, 8, v229
	v_cvt_f32_u32_e32 v229, v229
	v_rcp_f32_e32 v229, v229
	v_lshlrev_b32_e32 v124, 16, v48
	v_and_b32_e32 v125, 0xffff0000, v48
	v_lshlrev_b32_e32 v126, 16, v52
	v_and_b32_e32 v127, 0xffff0000, v52
	v_lshlrev_b32_e32 v128, 16, v56
	v_and_b32_e32 v129, 0xffff0000, v56
	v_lshlrev_b32_e32 v130, 16, v60
	v_and_b32_e32 v131, 0xffff0000, v60
	v_lshlrev_b32_e32 v132, 16, v64
	v_and_b32_e32 v133, 0xffff0000, v64
	v_lshlrev_b32_e32 v134, 16, v68
	v_and_b32_e32 v135, 0xffff0000, v68
	v_lshlrev_b32_e32 v136, 16, v72
	v_and_b32_e32 v137, 0xffff0000, v72
	v_lshlrev_b32_e32 v138, 16, v76
	v_and_b32_e32 v139, 0xffff0000, v76
	v_lshlrev_b32_e32 v140, 16, v80
	v_and_b32_e32 v141, 0xffff0000, v80
	v_lshlrev_b32_e32 v142, 16, v84
	v_and_b32_e32 v143, 0xffff0000, v84
	v_lshlrev_b32_e32 v144, 16, v88
	v_and_b32_e32 v145, 0xffff0000, v88
	v_add_f32_e32 v194, v124, v126
	v_add_f32_e32 v194, v194, v128
	v_add_f32_e32 v194, v194, v130
	v_add_f32_e32 v194, v194, v132
	v_add_f32_e32 v194, v194, v134
	v_add_f32_e32 v194, v194, v136
	v_add_f32_e32 v194, v194, v138
	v_fma_f32 v194, v194, v226, -v138
	v_add_f32_e32 v195, v125, v127
	v_add_f32_e32 v195, v195, v129
	v_add_f32_e32 v195, v195, v131
	v_add_f32_e32 v195, v195, v133
	v_add_f32_e32 v195, v195, v135
	v_add_f32_e32 v195, v195, v137
	v_add_f32_e32 v195, v195, v139
	v_fma_f32 v195, v195, v226, -v139
	v_add_f32_e32 v202, v126, v128
	v_add_f32_e32 v202, v202, v130
	v_add_f32_e32 v202, v202, v132
	v_add_f32_e32 v202, v202, v134
	v_add_f32_e32 v202, v202, v136
	v_add_f32_e32 v202, v202, v138
	v_add_f32_e32 v202, v202, v140
	v_fma_f32 v202, v202, v227, -v140
	v_add_f32_e32 v203, v127, v129
	v_add_f32_e32 v203, v203, v131
	v_add_f32_e32 v203, v203, v133
	v_add_f32_e32 v203, v203, v135
	v_add_f32_e32 v203, v203, v137
	v_add_f32_e32 v203, v203, v139
	v_add_f32_e32 v203, v203, v141
	v_fma_f32 v203, v203, v227, -v141
	v_add_f32_e32 v210, v128, v130
	v_add_f32_e32 v210, v210, v132
	v_add_f32_e32 v210, v210, v134
	v_add_f32_e32 v210, v210, v136
	v_add_f32_e32 v210, v210, v138
	v_add_f32_e32 v210, v210, v140
	v_add_f32_e32 v210, v210, v142
	v_fma_f32 v210, v210, v228, -v142
	v_add_f32_e32 v211, v129, v131
	v_add_f32_e32 v211, v211, v133
	v_add_f32_e32 v211, v211, v135
	v_add_f32_e32 v211, v211, v137
	v_add_f32_e32 v211, v211, v139
	v_add_f32_e32 v211, v211, v141
	v_add_f32_e32 v211, v211, v143
	v_fma_f32 v211, v211, v228, -v143
	v_add_f32_e32 v218, v130, v132
	v_add_f32_e32 v218, v218, v134
	v_add_f32_e32 v218, v218, v136
	v_add_f32_e32 v218, v218, v138
	v_add_f32_e32 v218, v218, v140
	v_add_f32_e32 v218, v218, v142
	v_add_f32_e32 v218, v218, v144
	v_fma_f32 v218, v218, v229, -v144
	v_add_f32_e32 v219, v131, v133
	v_add_f32_e32 v219, v219, v135
	v_add_f32_e32 v219, v219, v137
	v_add_f32_e32 v219, v219, v139
	v_add_f32_e32 v219, v219, v141
	v_add_f32_e32 v219, v219, v143
	v_add_f32_e32 v219, v219, v145
	v_fma_f32 v219, v219, v229, -v145
	v_lshlrev_b32_e32 v124, 16, v49
	v_and_b32_e32 v125, 0xffff0000, v49
	v_lshlrev_b32_e32 v126, 16, v53
	v_and_b32_e32 v127, 0xffff0000, v53
	v_lshlrev_b32_e32 v128, 16, v57
	v_and_b32_e32 v129, 0xffff0000, v57
	v_lshlrev_b32_e32 v130, 16, v61
	v_and_b32_e32 v131, 0xffff0000, v61
	v_lshlrev_b32_e32 v132, 16, v65
	v_and_b32_e32 v133, 0xffff0000, v65
	v_lshlrev_b32_e32 v134, 16, v69
	v_and_b32_e32 v135, 0xffff0000, v69
	v_lshlrev_b32_e32 v136, 16, v73
	v_and_b32_e32 v137, 0xffff0000, v73
	v_lshlrev_b32_e32 v138, 16, v77
	v_and_b32_e32 v139, 0xffff0000, v77
	v_lshlrev_b32_e32 v140, 16, v81
	v_and_b32_e32 v141, 0xffff0000, v81
	v_lshlrev_b32_e32 v142, 16, v85
	v_and_b32_e32 v143, 0xffff0000, v85
	v_lshlrev_b32_e32 v144, 16, v89
	v_and_b32_e32 v145, 0xffff0000, v89
	v_add_f32_e32 v196, v124, v126
	v_add_f32_e32 v196, v196, v128
	v_add_f32_e32 v196, v196, v130
	v_add_f32_e32 v196, v196, v132
	v_add_f32_e32 v196, v196, v134
	v_add_f32_e32 v196, v196, v136
	v_add_f32_e32 v196, v196, v138
	v_fma_f32 v196, v196, v226, -v138
	v_add_f32_e32 v197, v125, v127
	v_add_f32_e32 v197, v197, v129
	v_add_f32_e32 v197, v197, v131
	v_add_f32_e32 v197, v197, v133
	v_add_f32_e32 v197, v197, v135
	v_add_f32_e32 v197, v197, v137
	v_add_f32_e32 v197, v197, v139
	v_fma_f32 v197, v197, v226, -v139
	v_add_f32_e32 v204, v126, v128
	v_add_f32_e32 v204, v204, v130
	v_add_f32_e32 v204, v204, v132
	v_add_f32_e32 v204, v204, v134
	v_add_f32_e32 v204, v204, v136
	v_add_f32_e32 v204, v204, v138
	v_add_f32_e32 v204, v204, v140
	v_fma_f32 v204, v204, v227, -v140
	v_add_f32_e32 v205, v127, v129
	v_add_f32_e32 v205, v205, v131
	v_add_f32_e32 v205, v205, v133
	v_add_f32_e32 v205, v205, v135
	v_add_f32_e32 v205, v205, v137
	v_add_f32_e32 v205, v205, v139
	v_add_f32_e32 v205, v205, v141
	v_fma_f32 v205, v205, v227, -v141
	v_add_f32_e32 v212, v128, v130
	v_add_f32_e32 v212, v212, v132
	v_add_f32_e32 v212, v212, v134
	v_add_f32_e32 v212, v212, v136
	v_add_f32_e32 v212, v212, v138
	v_add_f32_e32 v212, v212, v140
	v_add_f32_e32 v212, v212, v142
	v_fma_f32 v212, v212, v228, -v142
	v_add_f32_e32 v213, v129, v131
	v_add_f32_e32 v213, v213, v133
	v_add_f32_e32 v213, v213, v135
	v_add_f32_e32 v213, v213, v137
	v_add_f32_e32 v213, v213, v139
	v_add_f32_e32 v213, v213, v141
	v_add_f32_e32 v213, v213, v143
	v_fma_f32 v213, v213, v228, -v143
	v_add_f32_e32 v220, v130, v132
	v_add_f32_e32 v220, v220, v134
	v_add_f32_e32 v220, v220, v136
	v_add_f32_e32 v220, v220, v138
	v_add_f32_e32 v220, v220, v140
	v_add_f32_e32 v220, v220, v142
; __device__ __forceinline__ unsigned pk2(float lo, float hi) { return pg8::cvt_pk_bf16(lo, hi); }
; __device__ __forceinline__ void unpack8(const v4u w, float (&f)[8]) { f[0] = bflo(w.x); f[1] = bfhi(w.x); f[2] = bflo(w.y); f[3] = bfhi(w.y); f[4] = bflo(w.z); f[5] = bfhi(w.z); f[6] = bflo(w.w); f[7] = bfhi(w.w); }
; template <int W> __device__ __forceinline__ void pool_item(Frame& F, int row, int t, int c8) {
;     ...
;     for (int k = 0; k < W; ++k) { const int kk = (t - k) >= 0 ? k : t; ld[k] = *(const v4u*)(F.PROJ + (size_t)(row - kk) * INWP + O_UPOOL + c8); }
; #pragma unroll
;     for (int k = W - 1; k >= 0; --k) { unpack8(ld[k], u); const float wgt = (t - k) >= 0 ? 1.f : 0.f;
; #pragma unroll
;         for (int i = 0; i < 8; ++i) s[i] += wgt * u[i]; }
;     const int cnt = (t + 1) < W ? (t + 1) : W;
;     const float inv = 1.0f / (float)cnt;
;     v4u o; o.x = pk2(s[0] * inv - u[0], s[1] * inv - u[1]); o.y = pk2(s[2] * inv - u[2], s[3] * inv - u[3]); o.z = pk2(s[4] * inv - u[4], s[5] * inv - u[5]); o.w = pk2(s[6] * inv - u[6], s[7] * inv - u[7]);
;     *(v4u*)(F.Y + (size_t)row * 1024 + c8) = o;
	v_add_f32_e32 v220, v220, v144
	v_fma_f32 v220, v220, v229, -v144
	v_add_f32_e32 v221, v131, v133
	v_add_f32_e32 v221, v221, v135
	v_add_f32_e32 v221, v221, v137
	v_add_f32_e32 v221, v221, v139
	v_add_f32_e32 v221, v221, v141
	v_add_f32_e32 v221, v221, v143
	v_add_f32_e32 v221, v221, v145
	v_fma_f32 v221, v221, v229, -v145
	v_lshlrev_b32_e32 v124, 16, v50
	v_and_b32_e32 v125, 0xffff0000, v50
	v_lshlrev_b32_e32 v126, 16, v54
	v_and_b32_e32 v127, 0xffff0000, v54
	v_lshlrev_b32_e32 v128, 16, v58
	v_and_b32_e32 v129, 0xffff0000, v58
	v_lshlrev_b32_e32 v130, 16, v62
	v_and_b32_e32 v131, 0xffff0000, v62
	v_lshlrev_b32_e32 v132, 16, v66
	v_and_b32_e32 v133, 0xffff0000, v66
	v_lshlrev_b32_e32 v134, 16, v70
	v_and_b32_e32 v135, 0xffff0000, v70
	v_lshlrev_b32_e32 v136, 16, v74
	v_and_b32_e32 v137, 0xffff0000, v74
	v_lshlrev_b32_e32 v138, 16, v78
	v_and_b32_e32 v139, 0xffff0000, v78
	v_lshlrev_b32_e32 v140, 16, v82
	v_and_b32_e32 v141, 0xffff0000, v82
	v_lshlrev_b32_e32 v142, 16, v86
	v_and_b32_e32 v143, 0xffff0000, v86
	v_lshlrev_b32_e32 v144, 16, v90
	v_and_b32_e32 v145, 0xffff0000, v90
	v_add_f32_e32 v198, v124, v126
	v_add_f32_e32 v198, v198, v128
	v_add_f32_e32 v198, v198, v130
	v_add_f32_e32 v198, v198, v132
	v_add_f32_e32 v198, v198, v134
	v_add_f32_e32 v198, v198, v136
	v_add_f32_e32 v198, v198, v138
	v_fma_f32 v198, v198, v226, -v138
	v_add_f32_e32 v199, v125, v127
	v_add_f32_e32 v199, v199, v129
	v_add_f32_e32 v199, v199, v131
	v_add_f32_e32 v199, v199, v133
	v_add_f32_e32 v199, v199, v135
	v_add_f32_e32 v199, v199, v137
	v_add_f32_e32 v199, v199, v139
	v_fma_f32 v199, v199, v226, -v139
	v_add_f32_e32 v206, v126, v128
	v_add_f32_e32 v206, v206, v130
	v_add_f32_e32 v206, v206, v132
	v_add_f32_e32 v206, v206, v134
	v_add_f32_e32 v206, v206, v136
	v_add_f32_e32 v206, v206, v138
	v_add_f32_e32 v206, v206, v140
	v_fma_f32 v206, v206, v227, -v140
	v_add_f32_e32 v207, v127, v129
	v_add_f32_e32 v207, v207, v131
	v_add_f32_e32 v207, v207, v133
	v_add_f32_e32 v207, v207, v135
	v_add_f32_e32 v207, v207, v137
	v_add_f32_e32 v207, v207, v139
	v_add_f32_e32 v207, v207, v141
	v_fma_f32 v207, v207, v227, -v141
	v_add_f32_e32 v214, v128, v130
	v_add_f32_e32 v214, v214, v132
	v_add_f32_e32 v214, v214, v134
	v_add_f32_e32 v214, v214, v136
	v_add_f32_e32 v214, v214, v138
	v_add_f32_e32 v214, v214, v140
	v_add_f32_e32 v214, v214, v142
	v_fma_f32 v214, v214, v228, -v142
	v_add_f32_e32 v215, v129, v131
	v_add_f32_e32 v215, v215, v133
	v_add_f32_e32 v215, v215, v135
	v_add_f32_e32 v215, v215, v137
	v_add_f32_e32 v215, v215, v139
	v_add_f32_e32 v215, v215, v141
	v_add_f32_e32 v215, v215, v143
	v_fma_f32 v215, v215, v228, -v143
	v_add_f32_e32 v222, v130, v132
	v_add_f32_e32 v222, v222, v134
	v_add_f32_e32 v222, v222, v136
	v_add_f32_e32 v222, v222, v138
	v_add_f32_e32 v222, v222, v140
	v_add_f32_e32 v222, v222, v142
	v_add_f32_e32 v222, v222, v144
	v_fma_f32 v222, v222, v229, -v144
	v_add_f32_e32 v223, v131, v133
	v_add_f32_e32 v223, v223, v135
	v_add_f32_e32 v223, v223, v137
	v_add_f32_e32 v223, v223, v139
	v_add_f32_e32 v223, v223, v141
	v_add_f32_e32 v223, v223, v143
	v_add_f32_e32 v223, v223, v145
	v_fma_f32 v223, v223, v229, -v145
	v_lshlrev_b32_e32 v124, 16, v51
	v_and_b32_e32 v125, 0xffff0000, v51
	v_lshlrev_b32_e32 v126, 16, v55
	v_and_b32_e32 v127, 0xffff0000, v55
	v_lshlrev_b32_e32 v128, 16, v59
	v_and_b32_e32 v129, 0xffff0000, v59
	v_lshlrev_b32_e32 v130, 16, v63
	v_and_b32_e32 v131, 0xffff0000, v63
	v_lshlrev_b32_e32 v132, 16, v67
	v_and_b32_e32 v133, 0xffff0000, v67
	v_lshlrev_b32_e32 v134, 16, v71
	v_and_b32_e32 v135, 0xffff0000, v71
	v_lshlrev_b32_e32 v136, 16, v75
	v_and_b32_e32 v137, 0xffff0000, v75
	v_lshlrev_b32_e32 v138, 16, v79
	v_and_b32_e32 v139, 0xffff0000, v79
	v_lshlrev_b32_e32 v140, 16, v83
	v_and_b32_e32 v141, 0xffff0000, v83
	v_lshlrev_b32_e32 v142, 16, v87
	v_and_b32_e32 v143, 0xffff0000, v87
	v_lshlrev_b32_e32 v144, 16, v91
	v_and_b32_e32 v145, 0xffff0000, v91
	v_add_f32_e32 v200, v124, v126
	v_add_f32_e32 v200, v200, v128
	v_add_f32_e32 v200, v200, v130
	v_add_f32_e32 v200, v200, v132
	v_add_f32_e32 v200, v200, v134
	v_add_f32_e32 v200, v200, v136
	v_add_f32_e32 v200, v200, v138
	v_fma_f32 v200, v200, v226, -v138
	v_add_f32_e32 v201, v125, v127
	v_add_f32_e32 v201, v201, v129
	v_add_f32_e32 v201, v201, v131
	v_add_f32_e32 v201, v201, v133
	v_add_f32_e32 v201, v201, v135
	v_add_f32_e32 v201, v201, v137
	v_add_f32_e32 v201, v201, v139
	v_fma_f32 v201, v201, v226, -v139
	v_add_f32_e32 v208, v126, v128
	v_add_f32_e32 v208, v208, v130
	v_add_f32_e32 v208, v208, v132
	v_add_f32_e32 v208, v208, v134
	v_add_f32_e32 v208, v208, v136
	v_add_f32_e32 v208, v208, v138
	v_add_f32_e32 v208, v208, v140
	v_fma_f32 v208, v208, v227, -v140
	v_add_f32_e32 v209, v127, v129
	v_add_f32_e32 v209, v209, v131
	v_add_f32_e32 v209, v209, v133
	v_add_f32_e32 v209, v209, v135
	v_add_f32_e32 v209, v209, v137
	v_add_f32_e32 v209, v209, v139
	v_add_f32_e32 v209, v209, v141
	v_fma_f32 v209, v209, v227, -v141
	v_add_f32_e32 v216, v128, v130
	v_add_f32_e32 v216, v216, v132
	v_add_f32_e32 v216, v216, v134
	v_add_f32_e32 v216, v216, v136
	v_add_f32_e32 v216, v216, v138
	v_add_f32_e32 v216, v216, v140
	v_add_f32_e32 v216, v216, v142
	v_fma_f32 v216, v216, v228, -v142
	v_add_f32_e32 v217, v129, v131
	v_add_f32_e32 v217, v217, v133
	v_add_f32_e32 v217, v217, v135
	v_add_f32_e32 v217, v217, v137
	v_add_f32_e32 v217, v217, v139
	v_add_f32_e32 v217, v217, v141
	v_add_f32_e32 v217, v217, v143
	v_fma_f32 v217, v217, v228, -v143
	v_add_f32_e32 v224, v130, v132
	v_add_f32_e32 v224, v224, v134
	v_add_f32_e32 v224, v224, v136
	v_add_f32_e32 v224, v224, v138
	v_add_f32_e32 v224, v224, v140
	v_add_f32_e32 v224, v224, v142
	v_add_f32_e32 v224, v224, v144
	v_fma_f32 v224, v224, v229, -v144
	v_add_f32_e32 v225, v131, v133
	v_add_f32_e32 v225, v225, v135
	v_add_f32_e32 v225, v225, v137
	v_add_f32_e32 v225, v225, v139
	v_add_f32_e32 v225, v225, v141
	v_add_f32_e32 v225, v225, v143
	v_add_f32_e32 v225, v225, v145
	v_fma_f32 v225, v225, v229, -v145
	v_cvt_pk_bf16_f32 v194, v194, v195
	v_cvt_pk_bf16_f32 v195, v196, v197
	v_cvt_pk_bf16_f32 v196, v198, v199
	v_cvt_pk_bf16_f32 v197, v200, v201
	global_store_dwordx4 v17, v[194:197], s[14:15]
	v_cvt_pk_bf16_f32 v202, v202, v203
	v_cvt_pk_bf16_f32 v203, v204, v205
	v_cvt_pk_bf16_f32 v204, v206, v207
	v_cvt_pk_bf16_f32 v205, v208, v209
	v_add_u32_e32 v13, 0x800, v17
	global_store_dwordx4 v13, v[202:205], s[14:15]
	v_cvt_pk_bf16_f32 v210, v210, v211
	v_cvt_pk_bf16_f32 v211, v212, v213
	v_cvt_pk_bf16_f32 v212, v214, v215
	v_cvt_pk_bf16_f32 v213, v216, v217
	v_add_u32_e32 v13, 0x1000, v17
	global_store_dwordx4 v13, v[210:213], s[14:15]
	v_cvt_pk_bf16_f32 v218, v218, v219
	v_cvt_pk_bf16_f32 v219, v220, v221
	v_cvt_pk_bf16_f32 v220, v222, v223
	v_cvt_pk_bf16_f32 v221, v224, v225
	v_add_u32_e32 v13, 0x1800, v17
	global_store_dwordx4 v13, v[218:221], s[14:15]
; __device__ __forceinline__ unsigned pk2(float lo, float hi) { return pg8::cvt_pk_bf16(lo, hi); }
; __device__ __forceinline__ void unpack8(const v4u w, float (&f)[8]) { f[0] = bflo(w.x); f[1] = bfhi(w.x); f[2] = bflo(w.y); f[3] = bfhi(w.y); f[4] = bflo(w.z); f[5] = bfhi(w.z); f[6] = bflo(w.w); f[7] = bfhi(w.w); }
; __device__ __forceinline__ void poolconv_phase(Frame& F, const float* conv_w_l) {
;     ...
;     for (int idx = gt; idx < M * 128; idx += NGT) {
;         const int row = idx >> 7, c8 = (idx & 127) * 8, t = row & (SEQ - 1);
;         float acc[8], a[8], b[8];
; #pragma unroll
;         for (int i = 0; i < 8; ++i) acc[i] = 0.f;
;         v4u la[3], lb[3];
; #pragma unroll
;         for (int j = 0; j < 3; ++j) { const int back = (t - 2 + j) >= 0 ? (2 - j) : 0; const bf16* pr = F.PROJ + (size_t)(row - back) * INWP; la[j] = *(const v4u*)(pr + O_CG + c8); lb[j] = *(const v4u*)(pr + O_UCONV + c8); }
;         const v4u lg = *(const v4u*)(F.PROJ + (size_t)row * INWP + O_BG + c8);
; #pragma unroll
;         for (int j = 0; j < 3; ++j) { const float wgt = (t - 2 + j) >= 0 ? 1.f : 0.f; unpack8(la[j], a); unpack8(lb[j], b);
;             const f32x4 w0 = *(const f32x4*)(conv_w_l + j * 1024 + c8) * wgt, w1 = *(const f32x4*)(conv_w_l + j * 1024 + c8 + 4) * wgt;
;             acc[0] += w0.x * (a[0] * b[0]); acc[1] += w0.y * (a[1] * b[1]); acc[2] += w0.z * (a[2] * b[2]); acc[3] += w0.w * (a[3] * b[3]);
;             acc[4] += w1.x * (a[4] * b[4]); acc[5] += w1.y * (a[5] * b[5]); acc[6] += w1.z * (a[6] * b[6]); acc[7] += w1.w * (a[7] * b[7]); }
;         unpack8(lg, a);
;         v4u o; o.x = pk2(a[0] * acc[0], a[1] * acc[1]); o.y = pk2(a[2] * acc[2], a[3] * acc[3]); o.z = pk2(a[4] * acc[4], a[5] * acc[5]); o.w = pk2(a[6] * acc[6], a[7] * acc[7]);
;         *(v4u*)(F.Y + (size_t)M * 1024 + (size_t)row * 1024 + c8) = o;
;     }
.Lpc_conv:
	s_mul_i32 s10, s10, 0x3000
	s_add_u32 s12, s86, s10
	s_addc_u32 s13, s87, 0
	v_and_b32_e32 v3, 0x7f, v1
	v_lshrrev_b32_e32 v2, 7, v1
	v_lshlrev_b32_e32 v8, 5, v3
	global_load_dwordx4 v[148:151], v8, s[12:13] offset:0
	global_load_dwordx4 v[152:155], v8, s[12:13] offset:16
	v_add_u32_e32 v8, 0x1000, v8
	global_load_dwordx4 v[156:159], v8, s[12:13] offset:0
	global_load_dwordx4 v[160:163], v8, s[12:13] offset:16
	v_add_u32_e32 v8, 0x1000, v8
	global_load_dwordx4 v[164:167], v8, s[12:13] offset:0
	global_load_dwordx4 v[168:171], v8, s[12:13] offset:16
	v_lshlrev_b32_e32 v8, 4, v3
	v_add_u32_e32 v19, 0x800, v8
	s_add_u32 s14, s14, 0x1000000
	s_addc_u32 s15, s15, 0
	v_lshlrev_b32_e32 v4, 2, v2
	v_and_b32_e32 v5, 0x7ff, v4
	v_mul_u32_u24_e32 v6, 0x3600, v5
	v_mul_u32_u24_e32 v7, 0x3600, v4
	v_add_u32_e32 v7, v7, v19
	v_lshl_add_u32 v16, v4, 11, v8
	v_min_u32_e32 v11, 0x6c00, v6
	v_sub_u32_e32 v12, v7, v11
	global_load_dwordx4 v[20:23], v12, s[96:97] offset:2048 nt
	global_load_dwordx4 v[44:47], v12, s[96:97] nt
	v_min_u32_e32 v11, 0x3600, v6
	v_sub_u32_e32 v12, v7, v11
	global_load_dwordx4 v[24:27], v12, s[96:97] offset:2048 nt
	global_load_dwordx4 v[48:51], v12, s[96:97] nt
	v_mov_b32_e32 v12, v7
	global_load_dwordx4 v[28:31], v12, s[96:97] offset:2048 nt
	global_load_dwordx4 v[52:55], v12, s[96:97] nt
	v_add_u32_e32 v13, 0x1000, v12
	global_load_dwordx4 v[68:71], v13, s[96:97] nt
	v_add_u32_e32 v12, 0x3600, v7
	global_load_dwordx4 v[32:35], v12, s[96:97] offset:2048 nt
	global_load_dwordx4 v[56:59], v12, s[96:97] nt
	v_add_u32_e32 v13, 0x1000, v12
	global_load_dwordx4 v[72:75], v13, s[96:97] nt
	v_add_u32_e32 v12, 0x6c00, v7
	global_load_dwordx4 v[36:39], v12, s[96:97] offset:2048 nt
	global_load_dwordx4 v[60:63], v12, s[96:97] nt
	v_add_u32_e32 v13, 0x1000, v12
	global_load_dwordx4 v[76:79], v13, s[96:97] nt
	v_add_u32_e32 v12, 0xa200, v7
	global_load_dwordx4 v[40:43], v12, s[96:97] offset:2048 nt
	global_load_dwordx4 v[64:67], v12, s[96:97] nt
	v_add_u32_e32 v13, 0x1000, v12
	global_load_dwordx4 v[80:83], v13, s[96:97] nt
	v_lshlrev_b32_e32 v4, 2, v2
	v_add_u32_e32 v4, 0x1000, v4
	v_and_b32_e32 v18, 0x7ff, v4
	v_mul_u32_u24_e32 v6, 0x3600, v18
	v_mul_u32_u24_e32 v7, 0x3600, v4
	v_add_u32_e32 v7, v7, v19
	v_lshl_add_u32 v17, v4, 11, v8
	v_min_u32_e32 v11, 0x6c00, v6
	v_sub_u32_e32 v12, v7, v11
	global_load_dwordx4 v[84:87], v12, s[96:97] offset:2048 nt
	global_load_dwordx4 v[108:111], v12, s[96:97] nt
	v_min_u32_e32 v11, 0x3600, v6
	v_sub_u32_e32 v12, v7, v11
	global_load_dwordx4 v[88:91], v12, s[96:97] offset:2048 nt
	global_load_dwordx4 v[112:115], v12, s[96:97] nt
	v_mov_b32_e32 v12, v7
	global_load_dwordx4 v[92:95], v12, s[96:97] offset:2048 nt
	global_load_dwordx4 v[116:119], v12, s[96:97] nt
	v_add_u32_e32 v13, 0x1000, v12
	global_load_dwordx4 v[132:135], v13, s[96:97] nt
	v_add_u32_e32 v12, 0x3600, v7
	global_load_dwordx4 v[96:99], v12, s[96:97] offset:2048 nt
	global_load_dwordx4 v[120:123], v12, s[96:97] nt
	v_add_u32_e32 v13, 0x1000, v12
	global_load_dwordx4 v[136:139], v13, s[96:97] nt
	v_add_u32_e32 v12, 0x6c00, v7
	global_load_dwordx4 v[100:103], v12, s[96:97] offset:2048 nt
	global_load_dwordx4 v[124:127], v12, s[96:97] nt
	v_add_u32_e32 v13, 0x1000, v12
	global_load_dwordx4 v[140:143], v13, s[96:97] nt
	v_add_u32_e32 v12, 0xa200, v7
	global_load_dwordx4 v[104:107], v12, s[96:97] offset:2048 nt
	global_load_dwordx4 v[128:131], v12, s[96:97] nt
	v_add_u32_e32 v13, 0x1000, v12
	global_load_dwordx4 v[144:147], v13, s[96:97] nt
	s_waitcnt vmcnt(16)
	v_cmp_le_u32_e32 vcc, 2, v5
	s_nop 1
	v_cndmask_b32_e32 v20, 0, v20, vcc
	v_cndmask_b32_e32 v21, 0, v21, vcc
	v_cndmask_b32_e32 v22, 0, v22, vcc
	v_cndmask_b32_e32 v23, 0, v23, vcc
	v_cmp_le_u32_e32 vcc, 1, v5
	s_nop 1
	v_cndmask_b32_e32 v24, 0, v24, vcc
	v_cndmask_b32_e32 v25, 0, v25, vcc
	v_cndmask_b32_e32 v26, 0, v26, vcc
	v_cndmask_b32_e32 v27, 0, v27, vcc
	v_lshlrev_b32_e32 v172, 16, v20
	v_and_b32_e32 v173, 0xffff0000, v20
	v_lshlrev_b32_e32 v174, 16, v44
	v_and_b32_e32 v175, 0xffff0000, v44
	v_mul_f32_e32 v194, v172, v174
	v_mul_f32_e32 v195, v173, v175
	v_lshlrev_b32_e32 v172, 16, v21
	v_and_b32_e32 v173, 0xffff0000, v21
	v_lshlrev_b32_e32 v174, 16, v45
	v_and_b32_e32 v175, 0xffff0000, v45
	v_mul_f32_e32 v196, v172, v174
	v_mul_f32_e32 v197, v173, v175
	v_lshlrev_b32_e32 v172, 16, v22
	v_and_b32_e32 v173, 0xffff0000, v22
	v_lshlrev_b32_e32 v174, 16, v46
	v_and_b32_e32 v175, 0xffff0000, v46
	v_mul_f32_e32 v198, v172, v174
	v_mul_f32_e32 v199, v173, v175
	v_lshlrev_b32_e32 v172, 16, v23
	v_and_b32_e32 v173, 0xffff0000, v23
	v_lshlrev_b32_e32 v174, 16, v47
	v_and_b32_e32 v175, 0xffff0000, v47
	v_mul_f32_e32 v200, v172, v174
	v_mul_f32_e32 v201, v173, v175
	v_lshlrev_b32_e32 v172, 16, v24
	v_and_b32_e32 v173, 0xffff0000, v24
	v_lshlrev_b32_e32 v174, 16, v48
	v_and_b32_e32 v175, 0xffff0000, v48
	v_mul_f32_e32 v202, v172, v174
	v_mul_f32_e32 v203, v173, v175
	v_lshlrev_b32_e32 v172, 16, v25
	v_and_b32_e32 v173, 0xffff0000, v25
	v_lshlrev_b32_e32 v174, 16, v49
	v_and_b32_e32 v175, 0xffff0000, v49
	v_mul_f32_e32 v204, v172, v174
	v_mul_f32_e32 v205, v173, v175
	v_lshlrev_b32_e32 v172, 16, v26
	v_and_b32_e32 v173, 0xffff0000, v26
	v_lshlrev_b32_e32 v174, 16, v50
	v_and_b32_e32 v175, 0xffff0000, v50
	v_mul_f32_e32 v206, v172, v174
	v_mul_f32_e32 v207, v173, v175
	v_lshlrev_b32_e32 v172, 16, v27
	v_and_b32_e32 v173, 0xffff0000, v27
	v_lshlrev_b32_e32 v174, 16, v51
	v_and_b32_e32 v175, 0xffff0000, v51
	v_mul_f32_e32 v208, v172, v174
	v_mul_f32_e32 v209, v173, v175
	v_lshlrev_b32_e32 v172, 16, v28
	v_and_b32_e32 v173, 0xffff0000, v28
	v_lshlrev_b32_e32 v174, 16, v52
; __device__ __forceinline__ unsigned pk2(float lo, float hi) { return pg8::cvt_pk_bf16(lo, hi); }
; __device__ __forceinline__ void unpack8(const v4u w, float (&f)[8]) { f[0] = bflo(w.x); f[1] = bfhi(w.x); f[2] = bflo(w.y); f[3] = bfhi(w.y); f[4] = bflo(w.z); f[5] = bfhi(w.z); f[6] = bflo(w.w); f[7] = bfhi(w.w); }
; __device__ __forceinline__ void poolconv_phase(Frame& F, const float* conv_w_l) {
;     ...
;         for (int j = 0; j < 3; ++j) { const float wgt = (t - 2 + j) >= 0 ? 1.f : 0.f; unpack8(la[j], a); unpack8(lb[j], b);
;             const f32x4 w0 = *(const f32x4*)(conv_w_l + j * 1024 + c8) * wgt, w1 = *(const f32x4*)(conv_w_l + j * 1024 + c8 + 4) * wgt;
;             acc[0] += w0.x * (a[0] * b[0]); acc[1] += w0.y * (a[1] * b[1]); acc[2] += w0.z * (a[2] * b[2]); acc[3] += w0.w * (a[3] * b[3]);
;             acc[4] += w1.x * (a[4] * b[4]); acc[5] += w1.y * (a[5] * b[5]); acc[6] += w1.z * (a[6] * b[6]); acc[7] += w1.w * (a[7] * b[7]); }
;         unpack8(lg, a);
;         v4u o; o.x = pk2(a[0] * acc[0], a[1] * acc[1]); o.y = pk2(a[2] * acc[2], a[3] * acc[3]); o.z = pk2(a[4] * acc[4], a[5] * acc[5]); o.w = pk2(a[6] * acc[6], a[7] * acc[7]);
	v_and_b32_e32 v175, 0xffff0000, v52
	v_mul_f32_e32 v210, v172, v174
	v_mul_f32_e32 v211, v173, v175
	v_lshlrev_b32_e32 v172, 16, v29
	v_and_b32_e32 v173, 0xffff0000, v29
	v_lshlrev_b32_e32 v174, 16, v53
	v_and_b32_e32 v175, 0xffff0000, v53
	v_mul_f32_e32 v212, v172, v174
	v_mul_f32_e32 v213, v173, v175
	v_lshlrev_b32_e32 v172, 16, v30
	v_and_b32_e32 v173, 0xffff0000, v30
	v_lshlrev_b32_e32 v174, 16, v54
	v_and_b32_e32 v175, 0xffff0000, v54
	v_mul_f32_e32 v214, v172, v174
	v_mul_f32_e32 v215, v173, v175
	v_lshlrev_b32_e32 v172, 16, v31
	v_and_b32_e32 v173, 0xffff0000, v31
	v_lshlrev_b32_e32 v174, 16, v55
	v_and_b32_e32 v175, 0xffff0000, v55
	v_mul_f32_e32 v216, v172, v174
	v_mul_f32_e32 v217, v173, v175
	v_lshlrev_b32_e32 v172, 16, v32
	v_and_b32_e32 v173, 0xffff0000, v32
	v_lshlrev_b32_e32 v174, 16, v56
	v_and_b32_e32 v175, 0xffff0000, v56
	v_mul_f32_e32 v218, v172, v174
	v_mul_f32_e32 v219, v173, v175
	v_lshlrev_b32_e32 v172, 16, v33
	v_and_b32_e32 v173, 0xffff0000, v33
	v_lshlrev_b32_e32 v174, 16, v57
	v_and_b32_e32 v175, 0xffff0000, v57
	v_mul_f32_e32 v220, v172, v174
	v_mul_f32_e32 v221, v173, v175
	v_lshlrev_b32_e32 v172, 16, v34
	v_and_b32_e32 v173, 0xffff0000, v34
	v_lshlrev_b32_e32 v174, 16, v58
	v_and_b32_e32 v175, 0xffff0000, v58
	v_mul_f32_e32 v222, v172, v174
	v_mul_f32_e32 v223, v173, v175
	v_lshlrev_b32_e32 v172, 16, v35
	v_and_b32_e32 v173, 0xffff0000, v35
	v_lshlrev_b32_e32 v174, 16, v59
	v_and_b32_e32 v175, 0xffff0000, v59
	v_mul_f32_e32 v224, v172, v174
	v_mul_f32_e32 v225, v173, v175
	v_lshlrev_b32_e32 v172, 16, v36
	v_and_b32_e32 v173, 0xffff0000, v36
	v_lshlrev_b32_e32 v174, 16, v60
	v_and_b32_e32 v175, 0xffff0000, v60
	v_mul_f32_e32 v226, v172, v174
	v_mul_f32_e32 v227, v173, v175
	v_lshlrev_b32_e32 v172, 16, v37
	v_and_b32_e32 v173, 0xffff0000, v37
	v_lshlrev_b32_e32 v174, 16, v61
	v_and_b32_e32 v175, 0xffff0000, v61
	v_mul_f32_e32 v228, v172, v174
	v_mul_f32_e32 v229, v173, v175
	v_lshlrev_b32_e32 v172, 16, v38
	v_and_b32_e32 v173, 0xffff0000, v38
	v_lshlrev_b32_e32 v174, 16, v62
	v_and_b32_e32 v175, 0xffff0000, v62
	v_mul_f32_e32 v230, v172, v174
	v_mul_f32_e32 v231, v173, v175
	v_lshlrev_b32_e32 v172, 16, v39
	v_and_b32_e32 v173, 0xffff0000, v39
	v_lshlrev_b32_e32 v174, 16, v63
	v_and_b32_e32 v175, 0xffff0000, v63
	v_mul_f32_e32 v232, v172, v174
	v_mul_f32_e32 v233, v173, v175
	v_lshlrev_b32_e32 v172, 16, v40
	v_and_b32_e32 v173, 0xffff0000, v40
	v_lshlrev_b32_e32 v174, 16, v64
	v_and_b32_e32 v175, 0xffff0000, v64
	v_mul_f32_e32 v234, v172, v174
	v_mul_f32_e32 v235, v173, v175
	v_lshlrev_b32_e32 v172, 16, v41
	v_and_b32_e32 v173, 0xffff0000, v41
	v_lshlrev_b32_e32 v174, 16, v65
	v_and_b32_e32 v175, 0xffff0000, v65
	v_mul_f32_e32 v236, v172, v174
	v_mul_f32_e32 v237, v173, v175
	v_lshlrev_b32_e32 v172, 16, v42
	v_and_b32_e32 v173, 0xffff0000, v42
	v_lshlrev_b32_e32 v174, 16, v66
	v_and_b32_e32 v175, 0xffff0000, v66
	v_mul_f32_e32 v238, v172, v174
	v_mul_f32_e32 v239, v173, v175
	v_lshlrev_b32_e32 v172, 16, v43
	v_and_b32_e32 v173, 0xffff0000, v43
	v_lshlrev_b32_e32 v174, 16, v67
	v_and_b32_e32 v175, 0xffff0000, v67
	v_mul_f32_e32 v240, v172, v174
	v_mul_f32_e32 v241, v173, v175
	v_lshlrev_b32_e32 v172, 16, v68
	v_and_b32_e32 v173, 0xffff0000, v68
	v_mul_f32_e32 v176, v148, v194
	v_fmac_f32_e32 v176, v156, v202
	v_fmac_f32_e32 v176, v164, v210
	v_mul_f32_e32 v176, v172, v176
	v_mul_f32_e32 v177, v149, v195
	v_fmac_f32_e32 v177, v157, v203
	v_fmac_f32_e32 v177, v165, v211
	v_mul_f32_e32 v177, v173, v177
	v_lshlrev_b32_e32 v172, 16, v69
	v_and_b32_e32 v173, 0xffff0000, v69
	v_mul_f32_e32 v178, v150, v196
	v_fmac_f32_e32 v178, v158, v204
	v_fmac_f32_e32 v178, v166, v212
	v_mul_f32_e32 v178, v172, v178
	v_mul_f32_e32 v179, v151, v197
	v_fmac_f32_e32 v179, v159, v205
	v_fmac_f32_e32 v179, v167, v213
	v_mul_f32_e32 v179, v173, v179
	v_lshlrev_b32_e32 v172, 16, v70
	v_and_b32_e32 v173, 0xffff0000, v70
	v_mul_f32_e32 v180, v152, v198
	v_fmac_f32_e32 v180, v160, v206
	v_fmac_f32_e32 v180, v168, v214
	v_mul_f32_e32 v180, v172, v180
	v_mul_f32_e32 v181, v153, v199
	v_fmac_f32_e32 v181, v161, v207
	v_fmac_f32_e32 v181, v169, v215
	v_mul_f32_e32 v181, v173, v181
	v_lshlrev_b32_e32 v172, 16, v71
	v_and_b32_e32 v173, 0xffff0000, v71
	v_mul_f32_e32 v182, v154, v200
	v_fmac_f32_e32 v182, v162, v208
	v_fmac_f32_e32 v182, v170, v216
	v_mul_f32_e32 v182, v172, v182
	v_mul_f32_e32 v183, v155, v201
	v_fmac_f32_e32 v183, v163, v209
	v_fmac_f32_e32 v183, v171, v217
	v_mul_f32_e32 v183, v173, v183
	v_cvt_pk_bf16_f32 v184, v176, v177
	v_cvt_pk_bf16_f32 v185, v178, v179
	v_cvt_pk_bf16_f32 v186, v180, v181
	v_cvt_pk_bf16_f32 v187, v182, v183
	global_store_dwordx4 v16, v[184:187], s[14:15]
	s_nop 1
	v_lshlrev_b32_e32 v172, 16, v72
	v_and_b32_e32 v173, 0xffff0000, v72
	v_mul_f32_e32 v176, v148, v202
	v_fmac_f32_e32 v176, v156, v210
	v_fmac_f32_e32 v176, v164, v218
	v_mul_f32_e32 v176, v172, v176
	v_mul_f32_e32 v177, v149, v203
	v_fmac_f32_e32 v177, v157, v211
	v_fmac_f32_e32 v177, v165, v219
	v_mul_f32_e32 v177, v173, v177
	v_lshlrev_b32_e32 v172, 16, v73
	v_and_b32_e32 v173, 0xffff0000, v73
	v_mul_f32_e32 v178, v150, v204
	v_fmac_f32_e32 v178, v158, v212
	v_fmac_f32_e32 v178, v166, v220
	v_mul_f32_e32 v178, v172, v178
	v_mul_f32_e32 v179, v151, v205
	v_fmac_f32_e32 v179, v159, v213
	v_fmac_f32_e32 v179, v167, v221
	v_mul_f32_e32 v179, v173, v179
	v_lshlrev_b32_e32 v172, 16, v74
	v_and_b32_e32 v173, 0xffff0000, v74
	v_mul_f32_e32 v180, v152, v206
	v_fmac_f32_e32 v180, v160, v214
	v_fmac_f32_e32 v180, v168, v222
	v_mul_f32_e32 v180, v172, v180
	v_mul_f32_e32 v181, v153, v207
	v_fmac_f32_e32 v181, v161, v215
	v_fmac_f32_e32 v181, v169, v223
; __device__ __forceinline__ unsigned pk2(float lo, float hi) { return pg8::cvt_pk_bf16(lo, hi); }
; __device__ __forceinline__ void unpack8(const v4u w, float (&f)[8]) { f[0] = bflo(w.x); f[1] = bfhi(w.x); f[2] = bflo(w.y); f[3] = bfhi(w.y); f[4] = bflo(w.z); f[5] = bfhi(w.z); f[6] = bflo(w.w); f[7] = bfhi(w.w); }
; __device__ __forceinline__ void poolconv_phase(Frame& F, const float* conv_w_l) {
;     ...
;         for (int j = 0; j < 3; ++j) { const float wgt = (t - 2 + j) >= 0 ? 1.f : 0.f; unpack8(la[j], a); unpack8(lb[j], b);
;             const f32x4 w0 = *(const f32x4*)(conv_w_l + j * 1024 + c8) * wgt, w1 = *(const f32x4*)(conv_w_l + j * 1024 + c8 + 4) * wgt;
;             acc[0] += w0.x * (a[0] * b[0]); acc[1] += w0.y * (a[1] * b[1]); acc[2] += w0.z * (a[2] * b[2]); acc[3] += w0.w * (a[3] * b[3]);
;             acc[4] += w1.x * (a[4] * b[4]); acc[5] += w1.y * (a[5] * b[5]); acc[6] += w1.z * (a[6] * b[6]); acc[7] += w1.w * (a[7] * b[7]); }
;         unpack8(lg, a);
;         v4u o; o.x = pk2(a[0] * acc[0], a[1] * acc[1]); o.y = pk2(a[2] * acc[2], a[3] * acc[3]); o.z = pk2(a[4] * acc[4], a[5] * acc[5]); o.w = pk2(a[6] * acc[6], a[7] * acc[7]);
;         *(v4u*)(F.Y + (size_t)M * 1024 + (size_t)row * 1024 + c8) = o;
	v_mul_f32_e32 v181, v173, v181
	v_lshlrev_b32_e32 v172, 16, v75
	v_and_b32_e32 v173, 0xffff0000, v75
	v_mul_f32_e32 v182, v154, v208
	v_fmac_f32_e32 v182, v162, v216
	v_fmac_f32_e32 v182, v170, v224
	v_mul_f32_e32 v182, v172, v182
	v_mul_f32_e32 v183, v155, v209
	v_fmac_f32_e32 v183, v163, v217
	v_fmac_f32_e32 v183, v171, v225
	v_mul_f32_e32 v183, v173, v183
	v_cvt_pk_bf16_f32 v184, v176, v177
	v_cvt_pk_bf16_f32 v185, v178, v179
	v_cvt_pk_bf16_f32 v186, v180, v181
	v_cvt_pk_bf16_f32 v187, v182, v183
	v_add_u32_e32 v13, 0x800, v16
	global_store_dwordx4 v13, v[184:187], s[14:15]
	s_nop 1
	v_lshlrev_b32_e32 v172, 16, v76
	v_and_b32_e32 v173, 0xffff0000, v76
	v_mul_f32_e32 v176, v148, v210
	v_fmac_f32_e32 v176, v156, v218
	v_fmac_f32_e32 v176, v164, v226
	v_mul_f32_e32 v176, v172, v176
	v_mul_f32_e32 v177, v149, v211
	v_fmac_f32_e32 v177, v157, v219
	v_fmac_f32_e32 v177, v165, v227
	v_mul_f32_e32 v177, v173, v177
	v_lshlrev_b32_e32 v172, 16, v77
	v_and_b32_e32 v173, 0xffff0000, v77
	v_mul_f32_e32 v178, v150, v212
	v_fmac_f32_e32 v178, v158, v220
	v_fmac_f32_e32 v178, v166, v228
	v_mul_f32_e32 v178, v172, v178
	v_mul_f32_e32 v179, v151, v213
	v_fmac_f32_e32 v179, v159, v221
	v_fmac_f32_e32 v179, v167, v229
	v_mul_f32_e32 v179, v173, v179
	v_lshlrev_b32_e32 v172, 16, v78
	v_and_b32_e32 v173, 0xffff0000, v78
	v_mul_f32_e32 v180, v152, v214
	v_fmac_f32_e32 v180, v160, v222
	v_fmac_f32_e32 v180, v168, v230
	v_mul_f32_e32 v180, v172, v180
	v_mul_f32_e32 v181, v153, v215
	v_fmac_f32_e32 v181, v161, v223
	v_fmac_f32_e32 v181, v169, v231
	v_mul_f32_e32 v181, v173, v181
	v_lshlrev_b32_e32 v172, 16, v79
	v_and_b32_e32 v173, 0xffff0000, v79
	v_mul_f32_e32 v182, v154, v216
	v_fmac_f32_e32 v182, v162, v224
	v_fmac_f32_e32 v182, v170, v232
	v_mul_f32_e32 v182, v172, v182
	v_mul_f32_e32 v183, v155, v217
	v_fmac_f32_e32 v183, v163, v225
	v_fmac_f32_e32 v183, v171, v233
	v_mul_f32_e32 v183, v173, v183
	v_cvt_pk_bf16_f32 v184, v176, v177
	v_cvt_pk_bf16_f32 v185, v178, v179
	v_cvt_pk_bf16_f32 v186, v180, v181
	v_cvt_pk_bf16_f32 v187, v182, v183
	v_add_u32_e32 v13, 0x1000, v16
	global_store_dwordx4 v13, v[184:187], s[14:15]
	s_nop 1
	v_lshlrev_b32_e32 v172, 16, v80
	v_and_b32_e32 v173, 0xffff0000, v80
	v_mul_f32_e32 v176, v148, v218
	v_fmac_f32_e32 v176, v156, v226
	v_fmac_f32_e32 v176, v164, v234
	v_mul_f32_e32 v176, v172, v176
	v_mul_f32_e32 v177, v149, v219
	v_fmac_f32_e32 v177, v157, v227
	v_fmac_f32_e32 v177, v165, v235
	v_mul_f32_e32 v177, v173, v177
	v_lshlrev_b32_e32 v172, 16, v81
	v_and_b32_e32 v173, 0xffff0000, v81
	v_mul_f32_e32 v178, v150, v220
	v_fmac_f32_e32 v178, v158, v228
	v_fmac_f32_e32 v178, v166, v236
	v_mul_f32_e32 v178, v172, v178
	v_mul_f32_e32 v179, v151, v221
	v_fmac_f32_e32 v179, v159, v229
	v_fmac_f32_e32 v179, v167, v237
	v_mul_f32_e32 v179, v173, v179
	v_lshlrev_b32_e32 v172, 16, v82
	v_and_b32_e32 v173, 0xffff0000, v82
	v_mul_f32_e32 v180, v152, v222
	v_fmac_f32_e32 v180, v160, v230
	v_fmac_f32_e32 v180, v168, v238
	v_mul_f32_e32 v180, v172, v180
	v_mul_f32_e32 v181, v153, v223
	v_fmac_f32_e32 v181, v161, v231
	v_fmac_f32_e32 v181, v169, v239
	v_mul_f32_e32 v181, v173, v181
	v_lshlrev_b32_e32 v172, 16, v83
	v_and_b32_e32 v173, 0xffff0000, v83
	v_mul_f32_e32 v182, v154, v224
	v_fmac_f32_e32 v182, v162, v232
	v_fmac_f32_e32 v182, v170, v240
	v_mul_f32_e32 v182, v172, v182
	v_mul_f32_e32 v183, v155, v225
	v_fmac_f32_e32 v183, v163, v233
	v_fmac_f32_e32 v183, v171, v241
	v_mul_f32_e32 v183, v173, v183
	v_cvt_pk_bf16_f32 v184, v176, v177
	v_cvt_pk_bf16_f32 v185, v178, v179
	v_cvt_pk_bf16_f32 v186, v180, v181
	v_cvt_pk_bf16_f32 v187, v182, v183
	v_add_u32_e32 v13, 0x1800, v16
	global_store_dwordx4 v13, v[184:187], s[14:15]
	s_nop 1
	s_waitcnt vmcnt(4)
	v_cmp_le_u32_e32 vcc, 2, v18
	s_nop 1
	v_cndmask_b32_e32 v84, 0, v84, vcc
	v_cndmask_b32_e32 v85, 0, v85, vcc
	v_cndmask_b32_e32 v86, 0, v86, vcc
	v_cndmask_b32_e32 v87, 0, v87, vcc
	v_cmp_le_u32_e32 vcc, 1, v18
	s_nop 1
	v_cndmask_b32_e32 v88, 0, v88, vcc
	v_cndmask_b32_e32 v89, 0, v89, vcc
	v_cndmask_b32_e32 v90, 0, v90, vcc
	v_cndmask_b32_e32 v91, 0, v91, vcc
	v_lshlrev_b32_e32 v172, 16, v84
	v_and_b32_e32 v173, 0xffff0000, v84
	v_lshlrev_b32_e32 v174, 16, v108
	v_and_b32_e32 v175, 0xffff0000, v108
	v_mul_f32_e32 v194, v172, v174
	v_mul_f32_e32 v195, v173, v175
	v_lshlrev_b32_e32 v172, 16, v85
	v_and_b32_e32 v173, 0xffff0000, v85
	v_lshlrev_b32_e32 v174, 16, v109
	v_and_b32_e32 v175, 0xffff0000, v109
	v_mul_f32_e32 v196, v172, v174
	v_mul_f32_e32 v197, v173, v175
	v_lshlrev_b32_e32 v172, 16, v86
	v_and_b32_e32 v173, 0xffff0000, v86
	v_lshlrev_b32_e32 v174, 16, v110
	v_and_b32_e32 v175, 0xffff0000, v110
	v_mul_f32_e32 v198, v172, v174
	v_mul_f32_e32 v199, v173, v175
	v_lshlrev_b32_e32 v172, 16, v87
	v_and_b32_e32 v173, 0xffff0000, v87
	v_lshlrev_b32_e32 v174, 16, v111
	v_and_b32_e32 v175, 0xffff0000, v111
	v_mul_f32_e32 v200, v172, v174
	v_mul_f32_e32 v201, v173, v175
	v_lshlrev_b32_e32 v172, 16, v88
	v_and_b32_e32 v173, 0xffff0000, v88
	v_lshlrev_b32_e32 v174, 16, v112
	v_and_b32_e32 v175, 0xffff0000, v112
	v_mul_f32_e32 v202, v172, v174
	v_mul_f32_e32 v203, v173, v175
	v_lshlrev_b32_e32 v172, 16, v89
	v_and_b32_e32 v173, 0xffff0000, v89
	v_lshlrev_b32_e32 v174, 16, v113
	v_and_b32_e32 v175, 0xffff0000, v113
	v_mul_f32_e32 v204, v172, v174
	v_mul_f32_e32 v205, v173, v175
	v_lshlrev_b32_e32 v172, 16, v90
	v_and_b32_e32 v173, 0xffff0000, v90
	v_lshlrev_b32_e32 v174, 16, v114
	v_and_b32_e32 v175, 0xffff0000, v114
	v_mul_f32_e32 v206, v172, v174
	v_mul_f32_e32 v207, v173, v175
	v_lshlrev_b32_e32 v172, 16, v91
	v_and_b32_e32 v173, 0xffff0000, v91
	v_lshlrev_b32_e32 v174, 16, v115
; __device__ __forceinline__ unsigned pk2(float lo, float hi) { return pg8::cvt_pk_bf16(lo, hi); }
; __device__ __forceinline__ void unpack8(const v4u w, float (&f)[8]) { f[0] = bflo(w.x); f[1] = bfhi(w.x); f[2] = bflo(w.y); f[3] = bfhi(w.y); f[4] = bflo(w.z); f[5] = bfhi(w.z); f[6] = bflo(w.w); f[7] = bfhi(w.w); }
; __device__ __forceinline__ void poolconv_phase(Frame& F, const float* conv_w_l) {
;     ...
;         for (int j = 0; j < 3; ++j) { const float wgt = (t - 2 + j) >= 0 ? 1.f : 0.f; unpack8(la[j], a); unpack8(lb[j], b);
;             const f32x4 w0 = *(const f32x4*)(conv_w_l + j * 1024 + c8) * wgt, w1 = *(const f32x4*)(conv_w_l + j * 1024 + c8 + 4) * wgt;
;             acc[0] += w0.x * (a[0] * b[0]); acc[1] += w0.y * (a[1] * b[1]); acc[2] += w0.z * (a[2] * b[2]); acc[3] += w0.w * (a[3] * b[3]);
;             acc[4] += w1.x * (a[4] * b[4]); acc[5] += w1.y * (a[5] * b[5]); acc[6] += w1.z * (a[6] * b[6]); acc[7] += w1.w * (a[7] * b[7]); }
;         unpack8(lg, a);
;         v4u o; o.x = pk2(a[0] * acc[0], a[1] * acc[1]); o.y = pk2(a[2] * acc[2], a[3] * acc[3]); o.z = pk2(a[4] * acc[4], a[5] * acc[5]); o.w = pk2(a[6] * acc[6], a[7] * acc[7]);
	v_and_b32_e32 v175, 0xffff0000, v115
	v_mul_f32_e32 v208, v172, v174
	v_mul_f32_e32 v209, v173, v175
	v_lshlrev_b32_e32 v172, 16, v92
	v_and_b32_e32 v173, 0xffff0000, v92
	v_lshlrev_b32_e32 v174, 16, v116
	v_and_b32_e32 v175, 0xffff0000, v116
	v_mul_f32_e32 v210, v172, v174
	v_mul_f32_e32 v211, v173, v175
	v_lshlrev_b32_e32 v172, 16, v93
	v_and_b32_e32 v173, 0xffff0000, v93
	v_lshlrev_b32_e32 v174, 16, v117
	v_and_b32_e32 v175, 0xffff0000, v117
	v_mul_f32_e32 v212, v172, v174
	v_mul_f32_e32 v213, v173, v175
	v_lshlrev_b32_e32 v172, 16, v94
	v_and_b32_e32 v173, 0xffff0000, v94
	v_lshlrev_b32_e32 v174, 16, v118
	v_and_b32_e32 v175, 0xffff0000, v118
	v_mul_f32_e32 v214, v172, v174
	v_mul_f32_e32 v215, v173, v175
	v_lshlrev_b32_e32 v172, 16, v95
	v_and_b32_e32 v173, 0xffff0000, v95
	v_lshlrev_b32_e32 v174, 16, v119
	v_and_b32_e32 v175, 0xffff0000, v119
	v_mul_f32_e32 v216, v172, v174
	v_mul_f32_e32 v217, v173, v175
	v_lshlrev_b32_e32 v172, 16, v96
	v_and_b32_e32 v173, 0xffff0000, v96
	v_lshlrev_b32_e32 v174, 16, v120
	v_and_b32_e32 v175, 0xffff0000, v120
	v_mul_f32_e32 v218, v172, v174
	v_mul_f32_e32 v219, v173, v175
	v_lshlrev_b32_e32 v172, 16, v97
	v_and_b32_e32 v173, 0xffff0000, v97
	v_lshlrev_b32_e32 v174, 16, v121
	v_and_b32_e32 v175, 0xffff0000, v121
	v_mul_f32_e32 v220, v172, v174
	v_mul_f32_e32 v221, v173, v175
	v_lshlrev_b32_e32 v172, 16, v98
	v_and_b32_e32 v173, 0xffff0000, v98
	v_lshlrev_b32_e32 v174, 16, v122
	v_and_b32_e32 v175, 0xffff0000, v122
	v_mul_f32_e32 v222, v172, v174
	v_mul_f32_e32 v223, v173, v175
	v_lshlrev_b32_e32 v172, 16, v99
	v_and_b32_e32 v173, 0xffff0000, v99
	v_lshlrev_b32_e32 v174, 16, v123
	v_and_b32_e32 v175, 0xffff0000, v123
	v_mul_f32_e32 v224, v172, v174
	v_mul_f32_e32 v225, v173, v175
	v_lshlrev_b32_e32 v172, 16, v100
	v_and_b32_e32 v173, 0xffff0000, v100
	v_lshlrev_b32_e32 v174, 16, v124
	v_and_b32_e32 v175, 0xffff0000, v124
	v_mul_f32_e32 v226, v172, v174
	v_mul_f32_e32 v227, v173, v175
	v_lshlrev_b32_e32 v172, 16, v101
	v_and_b32_e32 v173, 0xffff0000, v101
	v_lshlrev_b32_e32 v174, 16, v125
	v_and_b32_e32 v175, 0xffff0000, v125
	v_mul_f32_e32 v228, v172, v174
	v_mul_f32_e32 v229, v173, v175
	v_lshlrev_b32_e32 v172, 16, v102
	v_and_b32_e32 v173, 0xffff0000, v102
	v_lshlrev_b32_e32 v174, 16, v126
	v_and_b32_e32 v175, 0xffff0000, v126
	v_mul_f32_e32 v230, v172, v174
	v_mul_f32_e32 v231, v173, v175
	v_lshlrev_b32_e32 v172, 16, v103
	v_and_b32_e32 v173, 0xffff0000, v103
	v_lshlrev_b32_e32 v174, 16, v127
	v_and_b32_e32 v175, 0xffff0000, v127
	v_mul_f32_e32 v232, v172, v174
	v_mul_f32_e32 v233, v173, v175
	v_lshlrev_b32_e32 v172, 16, v104
	v_and_b32_e32 v173, 0xffff0000, v104
	v_lshlrev_b32_e32 v174, 16, v128
	v_and_b32_e32 v175, 0xffff0000, v128
	v_mul_f32_e32 v234, v172, v174
	v_mul_f32_e32 v235, v173, v175
	v_lshlrev_b32_e32 v172, 16, v105
	v_and_b32_e32 v173, 0xffff0000, v105
	v_lshlrev_b32_e32 v174, 16, v129
	v_and_b32_e32 v175, 0xffff0000, v129
	v_mul_f32_e32 v236, v172, v174
	v_mul_f32_e32 v237, v173, v175
	v_lshlrev_b32_e32 v172, 16, v106
	v_and_b32_e32 v173, 0xffff0000, v106
	v_lshlrev_b32_e32 v174, 16, v130
	v_and_b32_e32 v175, 0xffff0000, v130
	v_mul_f32_e32 v238, v172, v174
	v_mul_f32_e32 v239, v173, v175
	v_lshlrev_b32_e32 v172, 16, v107
	v_and_b32_e32 v173, 0xffff0000, v107
	v_lshlrev_b32_e32 v174, 16, v131
	v_and_b32_e32 v175, 0xffff0000, v131
	v_mul_f32_e32 v240, v172, v174
	v_mul_f32_e32 v241, v173, v175
	v_lshlrev_b32_e32 v172, 16, v132
	v_and_b32_e32 v173, 0xffff0000, v132
	v_mul_f32_e32 v176, v148, v194
	v_fmac_f32_e32 v176, v156, v202
	v_fmac_f32_e32 v176, v164, v210
	v_mul_f32_e32 v176, v172, v176
	v_mul_f32_e32 v177, v149, v195
	v_fmac_f32_e32 v177, v157, v203
	v_fmac_f32_e32 v177, v165, v211
	v_mul_f32_e32 v177, v173, v177
	v_lshlrev_b32_e32 v172, 16, v133
	v_and_b32_e32 v173, 0xffff0000, v133
	v_mul_f32_e32 v178, v150, v196
	v_fmac_f32_e32 v178, v158, v204
	v_fmac_f32_e32 v178, v166, v212
	v_mul_f32_e32 v178, v172, v178
	v_mul_f32_e32 v179, v151, v197
	v_fmac_f32_e32 v179, v159, v205
	v_fmac_f32_e32 v179, v167, v213
	v_mul_f32_e32 v179, v173, v179
	v_lshlrev_b32_e32 v172, 16, v134
	v_and_b32_e32 v173, 0xffff0000, v134
	v_mul_f32_e32 v180, v152, v198
	v_fmac_f32_e32 v180, v160, v206
	v_fmac_f32_e32 v180, v168, v214
	v_mul_f32_e32 v180, v172, v180
	v_mul_f32_e32 v181, v153, v199
	v_fmac_f32_e32 v181, v161, v207
	v_fmac_f32_e32 v181, v169, v215
	v_mul_f32_e32 v181, v173, v181
	v_lshlrev_b32_e32 v172, 16, v135
	v_and_b32_e32 v173, 0xffff0000, v135
	v_mul_f32_e32 v182, v154, v200
	v_fmac_f32_e32 v182, v162, v208
	v_fmac_f32_e32 v182, v170, v216
	v_mul_f32_e32 v182, v172, v182
	v_mul_f32_e32 v183, v155, v201
	v_fmac_f32_e32 v183, v163, v209
	v_fmac_f32_e32 v183, v171, v217
	v_mul_f32_e32 v183, v173, v183
	v_cvt_pk_bf16_f32 v184, v176, v177
	v_cvt_pk_bf16_f32 v185, v178, v179
	v_cvt_pk_bf16_f32 v186, v180, v181
; __device__ __forceinline__ unsigned pk2(float lo, float hi) { return pg8::cvt_pk_bf16(lo, hi); }
; __device__ __forceinline__ void unpack8(const v4u w, float (&f)[8]) { f[0] = bflo(w.x); f[1] = bfhi(w.x); f[2] = bflo(w.y); f[3] = bfhi(w.y); f[4] = bflo(w.z); f[5] = bfhi(w.z); f[6] = bflo(w.w); f[7] = bfhi(w.w); }
; __device__ __forceinline__ void poolconv_phase(Frame& F, const float* conv_w_l) {
;     ...
;         for (int j = 0; j < 3; ++j) { const float wgt = (t - 2 + j) >= 0 ? 1.f : 0.f; unpack8(la[j], a); unpack8(lb[j], b);
;             const f32x4 w0 = *(const f32x4*)(conv_w_l + j * 1024 + c8) * wgt, w1 = *(const f32x4*)(conv_w_l + j * 1024 + c8 + 4) * wgt;
;             acc[0] += w0.x * (a[0] * b[0]); acc[1] += w0.y * (a[1] * b[1]); acc[2] += w0.z * (a[2] * b[2]); acc[3] += w0.w * (a[3] * b[3]);
;             acc[4] += w1.x * (a[4] * b[4]); acc[5] += w1.y * (a[5] * b[5]); acc[6] += w1.z * (a[6] * b[6]); acc[7] += w1.w * (a[7] * b[7]); }
;         unpack8(lg, a);
;         v4u o; o.x = pk2(a[0] * acc[0], a[1] * acc[1]); o.y = pk2(a[2] * acc[2], a[3] * acc[3]); o.z = pk2(a[4] * acc[4], a[5] * acc[5]); o.w = pk2(a[6] * acc[6], a[7] * acc[7]);
;         *(v4u*)(F.Y + (size_t)M * 1024 + (size_t)row * 1024 + c8) = o;
	v_cvt_pk_bf16_f32 v187, v182, v183
	global_store_dwordx4 v17, v[184:187], s[14:15]
	s_nop 1
	v_lshlrev_b32_e32 v172, 16, v136
	v_and_b32_e32 v173, 0xffff0000, v136
	v_mul_f32_e32 v176, v148, v202
	v_fmac_f32_e32 v176, v156, v210
	v_fmac_f32_e32 v176, v164, v218
	v_mul_f32_e32 v176, v172, v176
	v_mul_f32_e32 v177, v149, v203
	v_fmac_f32_e32 v177, v157, v211
	v_fmac_f32_e32 v177, v165, v219
	v_mul_f32_e32 v177, v173, v177
	v_lshlrev_b32_e32 v172, 16, v137
	v_and_b32_e32 v173, 0xffff0000, v137
	v_mul_f32_e32 v178, v150, v204
	v_fmac_f32_e32 v178, v158, v212
	v_fmac_f32_e32 v178, v166, v220
	v_mul_f32_e32 v178, v172, v178
	v_mul_f32_e32 v179, v151, v205
	v_fmac_f32_e32 v179, v159, v213
	v_fmac_f32_e32 v179, v167, v221
	v_mul_f32_e32 v179, v173, v179
	v_lshlrev_b32_e32 v172, 16, v138
	v_and_b32_e32 v173, 0xffff0000, v138
	v_mul_f32_e32 v180, v152, v206
	v_fmac_f32_e32 v180, v160, v214
	v_fmac_f32_e32 v180, v168, v222
	v_mul_f32_e32 v180, v172, v180
	v_mul_f32_e32 v181, v153, v207
	v_fmac_f32_e32 v181, v161, v215
	v_fmac_f32_e32 v181, v169, v223
	v_mul_f32_e32 v181, v173, v181
	v_lshlrev_b32_e32 v172, 16, v139
	v_and_b32_e32 v173, 0xffff0000, v139
	v_mul_f32_e32 v182, v154, v208
	v_fmac_f32_e32 v182, v162, v216
	v_fmac_f32_e32 v182, v170, v224
	v_mul_f32_e32 v182, v172, v182
	v_mul_f32_e32 v183, v155, v209
	v_fmac_f32_e32 v183, v163, v217
	v_fmac_f32_e32 v183, v171, v225
	v_mul_f32_e32 v183, v173, v183
	v_cvt_pk_bf16_f32 v184, v176, v177
	v_cvt_pk_bf16_f32 v185, v178, v179
	v_cvt_pk_bf16_f32 v186, v180, v181
	v_cvt_pk_bf16_f32 v187, v182, v183
	v_add_u32_e32 v13, 0x800, v17
	global_store_dwordx4 v13, v[184:187], s[14:15]
	s_nop 1
	v_lshlrev_b32_e32 v172, 16, v140
	v_and_b32_e32 v173, 0xffff0000, v140
	v_mul_f32_e32 v176, v148, v210
	v_fmac_f32_e32 v176, v156, v218
	v_fmac_f32_e32 v176, v164, v226
	v_mul_f32_e32 v176, v172, v176
	v_mul_f32_e32 v177, v149, v211
	v_fmac_f32_e32 v177, v157, v219
	v_fmac_f32_e32 v177, v165, v227
	v_mul_f32_e32 v177, v173, v177
	v_lshlrev_b32_e32 v172, 16, v141
	v_and_b32_e32 v173, 0xffff0000, v141
	v_mul_f32_e32 v178, v150, v212
	v_fmac_f32_e32 v178, v158, v220
	v_fmac_f32_e32 v178, v166, v228
	v_mul_f32_e32 v178, v172, v178
	v_mul_f32_e32 v179, v151, v213
	v_fmac_f32_e32 v179, v159, v221
	v_fmac_f32_e32 v179, v167, v229
	v_mul_f32_e32 v179, v173, v179
	v_lshlrev_b32_e32 v172, 16, v142
	v_and_b32_e32 v173, 0xffff0000, v142
	v_mul_f32_e32 v180, v152, v214
	v_fmac_f32_e32 v180, v160, v222
	v_fmac_f32_e32 v180, v168, v230
	v_mul_f32_e32 v180, v172, v180
	v_mul_f32_e32 v181, v153, v215
	v_fmac_f32_e32 v181, v161, v223
	v_fmac_f32_e32 v181, v169, v231
	v_mul_f32_e32 v181, v173, v181
	v_lshlrev_b32_e32 v172, 16, v143
	v_and_b32_e32 v173, 0xffff0000, v143
	v_mul_f32_e32 v182, v154, v216
	v_fmac_f32_e32 v182, v162, v224
	v_fmac_f32_e32 v182, v170, v232
	v_mul_f32_e32 v182, v172, v182
	v_mul_f32_e32 v183, v155, v217
	v_fmac_f32_e32 v183, v163, v225
	v_fmac_f32_e32 v183, v171, v233
	v_mul_f32_e32 v183, v173, v183
	v_cvt_pk_bf16_f32 v184, v176, v177
	v_cvt_pk_bf16_f32 v185, v178, v179
	v_cvt_pk_bf16_f32 v186, v180, v181
	v_cvt_pk_bf16_f32 v187, v182, v183
	v_add_u32_e32 v13, 0x1000, v17
	global_store_dwordx4 v13, v[184:187], s[14:15]
	s_nop 1
	v_lshlrev_b32_e32 v172, 16, v144
	v_and_b32_e32 v173, 0xffff0000, v144
	v_mul_f32_e32 v176, v148, v218
	v_fmac_f32_e32 v176, v156, v226
	v_fmac_f32_e32 v176, v164, v234
	v_mul_f32_e32 v176, v172, v176
	v_mul_f32_e32 v177, v149, v219
	v_fmac_f32_e32 v177, v157, v227
	v_fmac_f32_e32 v177, v165, v235
	v_mul_f32_e32 v177, v173, v177
	v_lshlrev_b32_e32 v172, 16, v145
	v_and_b32_e32 v173, 0xffff0000, v145
	v_mul_f32_e32 v178, v150, v220
	v_fmac_f32_e32 v178, v158, v228
	v_fmac_f32_e32 v178, v166, v236
	v_mul_f32_e32 v178, v172, v178
	v_mul_f32_e32 v179, v151, v221
	v_fmac_f32_e32 v179, v159, v229
	v_fmac_f32_e32 v179, v167, v237
	v_mul_f32_e32 v179, v173, v179
	v_lshlrev_b32_e32 v172, 16, v146
	v_and_b32_e32 v173, 0xffff0000, v146
	v_mul_f32_e32 v180, v152, v222
	v_fmac_f32_e32 v180, v160, v230
	v_fmac_f32_e32 v180, v168, v238
	v_mul_f32_e32 v180, v172, v180
	v_mul_f32_e32 v181, v153, v223
	v_fmac_f32_e32 v181, v161, v231
	v_fmac_f32_e32 v181, v169, v239
	v_mul_f32_e32 v181, v173, v181
	v_lshlrev_b32_e32 v172, 16, v147
	v_and_b32_e32 v173, 0xffff0000, v147
	v_mul_f32_e32 v182, v154, v224
	v_fmac_f32_e32 v182, v162, v232
	v_fmac_f32_e32 v182, v170, v240
	v_mul_f32_e32 v182, v172, v182
	v_mul_f32_e32 v183, v155, v225
	v_fmac_f32_e32 v183, v163, v233
	v_fmac_f32_e32 v183, v171, v241
	v_mul_f32_e32 v183, v173, v183
	v_cvt_pk_bf16_f32 v184, v176, v177
	v_cvt_pk_bf16_f32 v185, v178, v179
	v_cvt_pk_bf16_f32 v186, v180, v181
	v_cvt_pk_bf16_f32 v187, v182, v183
	v_add_u32_e32 v13, 0x1800, v17
	global_store_dwordx4 v13, v[184:187], s[14:15]
	s_nop 1
	s_movk_i32 s8, 0x1000
	s_mov_b32 s20, 0xff800000
	s_mov_b64 s[2:3], exec
